# more weight conversions moved into idle GEMM-tail workgroups: DN2+OUT in P3 tail, BS5/BAT/BRW and UP2(l=0) in P1 tail; P0 shrinks
# speedup vs baseline: 1.0136x; 1.0136x over previous
; #define LAS __attribute__((address_space(3)))
; #define IN(k) in_range(lo, hi, (k))
; __global__ void __launch_bounds__(NWAVES * 64, 2) mk_fwd(Args args) {
;     ...
;     for (int l = 0; l < DEPTH; ++l) {
;         const int pb = 1 + l * NPH;
;         if (hi <= pb || lo >= pb + NPH) continue;
;         if (EN(0) && IN(pb + 0)) {
;             PH_LOCALS
;             LAS float* scr = (LAS float*)(lds + RING_OFF + wave * 16640);   static_assert(8 * 16640 <= LDSCTL_OFF, "converter scratch below the LDS control words");
;             constexpr int I_UP = (D / 64) * (NUP / 64), I_DN = (DFF / 64) * (D / 64), I_IN = (D / 64) * (DINP / 64), I_GLU = 16 * 16, I_L = 4 * 16, I_V1 = 16 * 4, I_V2 = 4 * 16,
;                           I_BS5 = 16 * 32, I_BAT = 8 * 32, I_BRW = 16 * 32, I_OUT = 32 * 32;
;             constexpr int NITEMS = 2 * I_UP + 2 * I_DN + I_IN + I_GLU + 3 * I_L + I_V1 + I_V2 + I_BS5 + I_BAT + I_BRW + I_OUT;
;             const int lv = l > 0 ? l - 1 : 0;
;     ...
;             for (int it = gw; it < NITEMS; it += NGW) {
.LBB0_25:
	s_mul_i32 s6, s58, 15
	s_add_i32 s2, s6, 1
	s_cmp_gt_i32 s77, s2
	s_cselect_b64 s[0:1], -1, 0
	s_add_i32 s3, s6, 16
	s_cmp_lt_i32 s76, s3
	s_cselect_b64 s[4:5], -1, 0
	s_and_b64 s[0:1], s[0:1], s[4:5]
	s_andn2_b64 vcc, exec, s[0:1]
	s_cbranch_vccnz .LBB0_24
	v_writelane_b32 v254, s6, 36
	v_writelane_b32 v254, s3, 37
	s_mov_b32 s3, s2
	s_cmp_gt_i32 s76, s3
	s_cselect_b64 s[0:1], -1, 0
	s_cmp_ge_i32 s3, s77
	s_cselect_b64 s[4:5], -1, 0
	s_or_b64 s[0:1], s[0:1], s[4:5]
	v_writelane_b32 v254, s58, 38
	s_and_b64 vcc, exec, s[0:1]
	s_cbranch_vccnz .LBB0_92
	s_movk_i32 s99, 0x1580
	v_readlane_b32 s0, v254, 8
	v_readlane_b32 s4, v254, 10
	v_readlane_b32 s1, v254, 9
	v_mbcnt_lo_u32_b32 v11, -1, 0
	v_mbcnt_hi_u32_b32 v11, -1, v11
	s_load_dword s6, s[0:1], 0x0
	s_mov_b32 s3, s84
	s_waitcnt lgkmcnt(0)
	s_lshl_b32 s3, s3, 3
	v_readlane_b32 s0, v254, 0
	s_add_i32 s3, s3, s4
	v_readlane_b32 s1, v254, 1
	s_cmp_ge_i32 s3, s99
	s_cbranch_scc1 .Lmy_p0_second
	s_load_dwordx2 s[8:9], s[0:1], 0x138
	v_readlane_b32 s14, v254, 38
	s_mulk_i32 s4, 0x4100
	s_add_i32 s7, s4, 0
	v_sub_u32_e64 v0, s14, 1 clamp
	s_lshl_b32 s33, s6, 3
	v_readfirstlane_b32 s4, v0
	s_lshl_b32 s96, s4, 16
	s_waitcnt lgkmcnt(0)
	s_add_u32 s4, s8, 0x22800000
	s_addc_u32 s5, s9, 0
	v_writelane_b32 v254, s4, 39
	s_mov_b32 s15, s97
	v_and_b32_e32 v0, 7, v11
	v_writelane_b32 v254, s5, 40
	s_add_u32 s4, s8, 0x22780000
	s_addc_u32 s5, s9, 0
	v_writelane_b32 v254, s4, 41
	v_ashrrev_i32_e32 v13, 3, v11
	v_lshlrev_b32_e32 v10, 3, v0
	v_writelane_b32 v254, s5, 42
	s_lshl_b32 s4, s14, 18
	s_add_u32 s10, s8, 0x22700000
	s_addc_u32 s11, s9, 0
	v_writelane_b32 v254, s10, 43
	s_mov_b32 s5, s97
	v_mul_u32_u24_e32 v0, 0x820, v0
	v_writelane_b32 v254, s11, 44
	s_mul_i32 s10, s14, 0x18000
	s_mov_b32 s11, s97
	v_writelane_b32 v254, s10, 45
	v_lshlrev_b32_e32 v1, 2, v13
	v_lshl_add_u32 v12, v11, 2, s7
	v_writelane_b32 v254, s11, 46
	s_add_u32 s10, s8, 0x22680000
	s_addc_u32 s11, s9, 0
	v_writelane_b32 v254, s10, 47
	v_add3_u32 v14, s7, v0, v1
	s_mov_b32 s41, s97
	v_writelane_b32 v254, s11, 48
	s_add_u32 s10, s8, 0x22600000
	s_addc_u32 s11, s9, 0
	v_writelane_b32 v254, s10, 49
	s_nop 1
	v_writelane_b32 v254, s11, 50
	s_lshl_b32 s10, s14, 20
	s_mov_b32 s11, s97
	v_writelane_b32 v254, s10, 51
	s_nop 1
	v_writelane_b32 v254, s11, 52
	s_add_u32 s10, s8, 0x22400000
	s_addc_u32 s11, s9, 0
	v_writelane_b32 v254, s10, 53
	s_nop 1
	v_writelane_b32 v254, s11, 54
	s_lshl_b32 s10, s14, 21
	s_mov_b32 s11, s97
	v_writelane_b32 v254, s10, 55
	s_nop 1
	v_writelane_b32 v254, s11, 56
	s_add_u32 s10, s8, 0x22e80000
	s_addc_u32 s11, s9, 0
	v_writelane_b32 v254, s10, 57
	s_nop 1
	v_writelane_b32 v254, s11, 58
	s_add_u32 s10, s8, 0x27b80000
	s_addc_u32 s11, s9, 0
	v_writelane_b32 v254, s10, 59
	s_nop 1
	v_writelane_b32 v254, s11, 60
	s_add_u32 s10, s8, 0x22880000
	s_addc_u32 s11, s9, 0
	v_writelane_b32 v254, s10, 61
	s_nop 1
	v_writelane_b32 v254, s11, 62
	s_lshl_b32 s10, s14, 22
	s_add_u32 s12, s8, 0x23280000
	s_addc_u32 s13, s9, 0
	v_writelane_b32 v254, s12, 63
	s_mov_b32 s11, s97
	s_nop 0
	v_writelane_b32 v255, s13, 0
	s_mul_i32 s12, s14, 0xac0000
	s_mov_b32 s13, s97
	v_writelane_b32 v255, s12, 1
	s_nop 1
	v_writelane_b32 v255, s13, 2
	s_add_u32 s12, s8, 0x26580000
	s_addc_u32 s13, s9, 0
	v_writelane_b32 v255, s12, 3
	s_nop 1
	v_writelane_b32 v255, s13, 4
	s_add_u32 s12, s8, 0x1d200000
	s_addc_u32 s13, s9, 0
	s_lshl_b32 s40, s14, 11
	v_writelane_b32 v255, s12, 5
	s_add_u32 s16, s8, 0x1e800000
	s_addc_u32 s17, s9, 0
	v_writelane_b32 v255, s13, 6
	v_writelane_b32 v255, s16, 7
	s_mul_i32 s12, s14, 0x1de0000
	s_mul_i32 s14, s14, 0x1580000
	v_writelane_b32 v255, s17, 8
	v_writelane_b32 v255, s14, 9
	s_mov_b32 s13, s97
	s_nop 0
	v_writelane_b32 v255, s15, 10
	s_add_u32 s14, s8, 0x23a80000
	s_addc_u32 s15, s9, 0
	v_writelane_b32 v255, s14, 11
	s_add_u32 s8, s8, 0x1a700000
	s_addc_u32 s9, s9, 0
	v_writelane_b32 v255, s15, 12
	v_writelane_b32 v255, s8, 13
	s_lshl_b64 s[4:5], s[4:5], 2
	s_lshl_b32 s7, s3, 4
	v_writelane_b32 v255, s9, 14
	v_writelane_b32 v255, s4, 15
	s_add_i32 s72, s7, 0xc00
	s_lshl_b32 s7, s3, 1
	v_writelane_b32 v255, s5, 16
	s_lshl_b64 s[4:5], s[10:11], 2
	v_writelane_b32 v255, s4, 17
	s_lshl_b32 s66, s3, 6
	s_lshl_b32 s67, s6, 9
	v_writelane_b32 v255, s5, 18
	s_lshl_b64 s[4:5], s[12:13], 2
	v_writelane_b32 v255, s4, 19
	s_lshl_b32 s68, s3, 5
	s_lshl_b32 s69, s6, 8
	v_writelane_b32 v255, s5, 20
	v_writelane_b32 v255, s80, 21
	s_lshl_b32 s70, s3, 2
	s_lshl_b32 s71, s6, 5
	v_writelane_b32 v255, s81, 22
	v_writelane_b32 v255, s82, 23
	s_lshl_b32 s73, s6, 7
	s_add_i32 s74, s7, 0x13500
	s_lshl_b32 s75, s6, 4
	v_writelane_b32 v255, s83, 24
	s_branch .LBB0_31

; #define LAS __attribute__((address_space(3)))
; __global__ void __launch_bounds__(NWAVES * 64, 2) mk_fwd(Args args) {
;     ...
;             LAS float* scr = (LAS float*)(lds + RING_OFF + wave * 16640);   static_assert(8 * 16640 <= LDSCTL_OFF, "converter scratch below the LDS control words");
;             constexpr int I_UP = (D / 64) * (NUP / 64), I_DN = (DFF / 64) * (D / 64), I_IN = (D / 64) * (DINP / 64), I_GLU = 16 * 16, I_L = 4 * 16, I_V1 = 16 * 4, I_V2 = 4 * 16,
;                           I_BS5 = 16 * 32, I_BAT = 8 * 32, I_BRW = 16 * 32, I_OUT = 32 * 32;
;             constexpr int NITEMS = 2 * I_UP + 2 * I_DN + I_IN + I_GLU + 3 * I_L + I_V1 + I_V2 + I_BS5 + I_BAT + I_BRW + I_OUT;
;             const int lv = l > 0 ? l - 1 : 0;
;     ...
;             for (int it = gw; it < NITEMS; it += NGW) {
;                 ConvItem ca; CONV_DESC(ca, it);
;                 float va[64];
;                 conv_load(ca, lane, va);
;                 conv_store(ca, scr, lane, va);
;             }
.Lmy_p0_second:
	v_readlane_b32 s0, v254, 8
	v_readlane_b32 s4, v254, 10
	v_readlane_b32 s1, v254, 9
	v_mbcnt_lo_u32_b32 v11, -1, 0
	v_mbcnt_hi_u32_b32 v11, -1, v11
	s_load_dword s6, s[0:1], 0x0
	s_mov_b32 s3, s84
	s_waitcnt lgkmcnt(0)
	s_movk_i32 s6, 256
	s_lshl_b32 s3, s3, 3
	v_readlane_b32 s0, v254, 0
	s_add_i32 s3, s3, s4
	s_add_i32 s3, s3, 0x6780
	v_readlane_b32 s1, v254, 1
	s_cmpk_gt_i32 s3, 27071
	s_cbranch_scc1 .Lcvp0b_ret
	s_load_dwordx2 s[8:9], s[0:1], 0x138
	v_readlane_b32 s14, v254, 38
	s_mulk_i32 s4, 0x4100
	s_add_i32 s7, s4, 0
	v_sub_u32_e64 v0, s14, 1 clamp
	s_lshl_b32 s33, s6, 3
	v_readfirstlane_b32 s4, v0
	s_lshl_b32 s96, s4, 16
	s_waitcnt lgkmcnt(0)
	s_add_u32 s4, s8, 0x22800000
	s_addc_u32 s5, s9, 0
	v_writelane_b32 v254, s4, 39
	s_mov_b32 s15, s97
	v_and_b32_e32 v0, 7, v11
	v_writelane_b32 v254, s5, 40
	s_add_u32 s4, s8, 0x22780000
	s_addc_u32 s5, s9, 0
	v_writelane_b32 v254, s4, 41
	v_ashrrev_i32_e32 v13, 3, v11
	v_lshlrev_b32_e32 v10, 3, v0
	v_writelane_b32 v254, s5, 42
	s_lshl_b32 s4, s14, 18
	s_add_u32 s10, s8, 0x22700000
	s_addc_u32 s11, s9, 0
	v_writelane_b32 v254, s10, 43
	s_mov_b32 s5, s97
	v_mul_u32_u24_e32 v0, 0x820, v0
	v_writelane_b32 v254, s11, 44
	s_mul_i32 s10, s14, 0x18000
	s_mov_b32 s11, s97
	v_writelane_b32 v254, s10, 45
	v_lshlrev_b32_e32 v1, 2, v13
	v_lshl_add_u32 v12, v11, 2, s7
	v_writelane_b32 v254, s11, 46
	s_add_u32 s10, s8, 0x22680000
	s_addc_u32 s11, s9, 0
	v_writelane_b32 v254, s10, 47
	v_add3_u32 v14, s7, v0, v1
	s_mov_b32 s41, s97
	v_writelane_b32 v254, s11, 48
	s_add_u32 s10, s8, 0x22600000
	s_addc_u32 s11, s9, 0
	v_writelane_b32 v254, s10, 49
	s_nop 1
	v_writelane_b32 v254, s11, 50
	s_lshl_b32 s10, s14, 20
	s_mov_b32 s11, s97
	v_writelane_b32 v254, s10, 51
	s_nop 1
	v_writelane_b32 v254, s11, 52
	s_add_u32 s10, s8, 0x22400000
	s_addc_u32 s11, s9, 0
	v_writelane_b32 v254, s10, 53
	s_nop 1
	v_writelane_b32 v254, s11, 54
	s_lshl_b32 s10, s14, 21
	s_mov_b32 s11, s97
	v_writelane_b32 v254, s10, 55
	s_nop 1
	v_writelane_b32 v254, s11, 56
	s_add_u32 s10, s8, 0x22e80000
	s_addc_u32 s11, s9, 0
	v_writelane_b32 v254, s10, 57
	s_nop 1
	v_writelane_b32 v254, s11, 58
	s_add_u32 s10, s8, 0x27b80000
	s_addc_u32 s11, s9, 0
	v_writelane_b32 v254, s10, 59
	s_nop 1
	v_writelane_b32 v254, s11, 60
	s_add_u32 s10, s8, 0x22880000
	s_addc_u32 s11, s9, 0
	v_writelane_b32 v254, s10, 61
	s_nop 1
	v_writelane_b32 v254, s11, 62
	s_lshl_b32 s10, s14, 22
	s_add_u32 s12, s8, 0x23280000
	s_addc_u32 s13, s9, 0
	v_writelane_b32 v254, s12, 63
	s_mov_b32 s11, s97
	s_nop 0
	v_writelane_b32 v255, s13, 0
	s_mul_i32 s12, s14, 0xac0000
	s_mov_b32 s13, s97
	v_writelane_b32 v255, s12, 1
	s_nop 1
	v_writelane_b32 v255, s13, 2
	s_add_u32 s12, s8, 0x26580000
	s_addc_u32 s13, s9, 0
	v_writelane_b32 v255, s12, 3
	s_nop 1
	v_writelane_b32 v255, s13, 4
	s_add_u32 s12, s8, 0x1d200000
	s_addc_u32 s13, s9, 0
	s_lshl_b32 s40, s14, 11
	v_writelane_b32 v255, s12, 5
	s_add_u32 s16, s8, 0x1e800000
	s_addc_u32 s17, s9, 0
	v_writelane_b32 v255, s13, 6
	v_writelane_b32 v255, s16, 7
	s_mul_i32 s12, s14, 0x1de0000
	s_mul_i32 s14, s14, 0x1580000
	v_writelane_b32 v255, s17, 8
	v_writelane_b32 v255, s14, 9
	s_mov_b32 s13, s97
	s_nop 0
	v_writelane_b32 v255, s15, 10
	s_add_u32 s14, s8, 0x23a80000
	s_addc_u32 s15, s9, 0
	v_writelane_b32 v255, s14, 11
	s_add_u32 s8, s8, 0x1a700000
	s_addc_u32 s9, s9, 0
	v_writelane_b32 v255, s15, 12
	v_writelane_b32 v255, s8, 13
	s_lshl_b64 s[4:5], s[4:5], 2
	s_lshl_b32 s7, s3, 4
	v_writelane_b32 v255, s9, 14
	v_writelane_b32 v255, s4, 15
	s_add_i32 s72, s7, 0xc00
	s_lshl_b32 s7, s3, 1
	v_writelane_b32 v255, s5, 16
	s_lshl_b64 s[4:5], s[10:11], 2
	v_writelane_b32 v255, s4, 17
	s_lshl_b32 s66, s3, 6
	s_lshl_b32 s67, s6, 9
	v_writelane_b32 v255, s5, 18
	s_lshl_b64 s[4:5], s[12:13], 2
	v_writelane_b32 v255, s4, 19
	s_lshl_b32 s68, s3, 5
	s_lshl_b32 s69, s6, 8
	v_writelane_b32 v255, s5, 20
	v_writelane_b32 v255, s80, 21
	s_lshl_b32 s70, s3, 2
	s_lshl_b32 s71, s6, 5
	v_writelane_b32 v255, s81, 22
	v_writelane_b32 v255, s82, 23
	s_lshl_b32 s73, s6, 7
	s_add_i32 s74, s7, 0x13500
	s_lshl_b32 s75, s6, 4
	v_writelane_b32 v255, s83, 24
	s_branch .Lcvp0b_31

; #define LAS __attribute__((address_space(3)))
; __global__ void __launch_bounds__(NWAVES * 64, 2) mk_fwd(Args args) {
;     ...
;             LAS float* scr = (LAS float*)(lds + RING_OFF + wave * 16640);   static_assert(8 * 16640 <= LDSCTL_OFF, "converter scratch below the LDS control words");
;             constexpr int I_UP = (D / 64) * (NUP / 64), I_DN = (DFF / 64) * (D / 64), I_IN = (D / 64) * (DINP / 64), I_GLU = 16 * 16, I_L = 4 * 16, I_V1 = 16 * 4, I_V2 = 4 * 16,
;                           I_BS5 = 16 * 32, I_BAT = 8 * 32, I_BRW = 16 * 32, I_OUT = 32 * 32;
;             constexpr int NITEMS = 2 * I_UP + 2 * I_DN + I_IN + I_GLU + 3 * I_L + I_V1 + I_V2 + I_BS5 + I_BAT + I_BRW + I_OUT;
;             const int lv = l > 0 ? l - 1 : 0;
;     ...
;             for (int it = gw; it < NITEMS; it += NGW) {
;                 ConvItem ca; CONV_DESC(ca, it);
;                 float va[64];
;                 conv_load(ca, lane, va);
;                 conv_store(ca, scr, lane, va);
;             }
.Lcvp0b_ret:
	v_readlane_b32 s98, v254, 38
	s_nop 3
	s_cmp_gt_u32 s98, 0
	s_cbranch_scc1 .LBB0_92
	v_readlane_b32 s0, v254, 8
	v_readlane_b32 s4, v254, 10
	v_readlane_b32 s1, v254, 9
	v_mbcnt_lo_u32_b32 v11, -1, 0
	v_mbcnt_hi_u32_b32 v11, -1, v11
	s_load_dword s6, s[0:1], 0x0
	s_mov_b32 s3, s84
	s_waitcnt lgkmcnt(0)
	s_movk_i32 s6, 256
	s_lshl_b32 s3, s3, 3
	v_readlane_b32 s0, v254, 0
	s_add_i32 s3, s3, s4
	s_add_i32 s3, s3, 0x2b00
	v_readlane_b32 s1, v254, 1
	s_cmpk_gt_i32 s3, 21439
	s_cbranch_scc1 .Lcvp0c_ret
	s_load_dwordx2 s[8:9], s[0:1], 0x138
	v_readlane_b32 s14, v254, 38
	s_mulk_i32 s4, 0x4100
	s_add_i32 s7, s4, 0
	v_sub_u32_e64 v0, s14, 1 clamp
	s_lshl_b32 s33, s6, 3
	v_readfirstlane_b32 s4, v0
	s_lshl_b32 s96, s4, 16
	s_waitcnt lgkmcnt(0)
	s_add_u32 s4, s8, 0x22800000
	s_addc_u32 s5, s9, 0
	v_writelane_b32 v254, s4, 39
	s_mov_b32 s15, s97
	v_and_b32_e32 v0, 7, v11
	v_writelane_b32 v254, s5, 40
	s_add_u32 s4, s8, 0x22780000
	s_addc_u32 s5, s9, 0
	v_writelane_b32 v254, s4, 41
	v_ashrrev_i32_e32 v13, 3, v11
	v_lshlrev_b32_e32 v10, 3, v0
	v_writelane_b32 v254, s5, 42
	s_lshl_b32 s4, s14, 18
	s_add_u32 s10, s8, 0x22700000
	s_addc_u32 s11, s9, 0
	v_writelane_b32 v254, s10, 43
	s_mov_b32 s5, s97
	v_mul_u32_u24_e32 v0, 0x820, v0
	v_writelane_b32 v254, s11, 44
	s_mul_i32 s10, s14, 0x18000
	s_mov_b32 s11, s97
	v_writelane_b32 v254, s10, 45
	v_lshlrev_b32_e32 v1, 2, v13
	v_lshl_add_u32 v12, v11, 2, s7
	v_writelane_b32 v254, s11, 46
	s_add_u32 s10, s8, 0x22680000
	s_addc_u32 s11, s9, 0
	v_writelane_b32 v254, s10, 47
	v_add3_u32 v14, s7, v0, v1
	s_mov_b32 s41, s97
	v_writelane_b32 v254, s11, 48
	s_add_u32 s10, s8, 0x22600000
	s_addc_u32 s11, s9, 0
	v_writelane_b32 v254, s10, 49
	s_nop 1
	v_writelane_b32 v254, s11, 50
	s_lshl_b32 s10, s14, 20
	s_mov_b32 s11, s97
	v_writelane_b32 v254, s10, 51
	s_nop 1
	v_writelane_b32 v254, s11, 52
	s_add_u32 s10, s8, 0x22400000
	s_addc_u32 s11, s9, 0
	v_writelane_b32 v254, s10, 53
	s_nop 1
	v_writelane_b32 v254, s11, 54
	s_lshl_b32 s10, s14, 21
	s_mov_b32 s11, s97
	v_writelane_b32 v254, s10, 55
	s_nop 1
	v_writelane_b32 v254, s11, 56
	s_add_u32 s10, s8, 0x22e80000
	s_addc_u32 s11, s9, 0
	v_writelane_b32 v254, s10, 57
	s_nop 1
	v_writelane_b32 v254, s11, 58
	s_add_u32 s10, s8, 0x27b80000
	s_addc_u32 s11, s9, 0
	v_writelane_b32 v254, s10, 59
	s_nop 1
	v_writelane_b32 v254, s11, 60
	s_add_u32 s10, s8, 0x22880000
	s_addc_u32 s11, s9, 0
	v_writelane_b32 v254, s10, 61
	s_nop 1
	v_writelane_b32 v254, s11, 62
	s_lshl_b32 s10, s14, 22
	s_add_u32 s12, s8, 0x23280000
	s_addc_u32 s13, s9, 0
	v_writelane_b32 v254, s12, 63
	s_mov_b32 s11, s97
	s_nop 0
	v_writelane_b32 v255, s13, 0
	s_mul_i32 s12, s14, 0xac0000
	s_mov_b32 s13, s97
	v_writelane_b32 v255, s12, 1
	s_nop 1
	v_writelane_b32 v255, s13, 2
	s_add_u32 s12, s8, 0x26580000
	s_addc_u32 s13, s9, 0
	v_writelane_b32 v255, s12, 3
	s_nop 1
	v_writelane_b32 v255, s13, 4
	s_add_u32 s12, s8, 0x1d200000
	s_addc_u32 s13, s9, 0
	s_lshl_b32 s40, s14, 11
	v_writelane_b32 v255, s12, 5
	s_add_u32 s16, s8, 0x1e800000
	s_addc_u32 s17, s9, 0
	v_writelane_b32 v255, s13, 6
	v_writelane_b32 v255, s16, 7
	s_mul_i32 s12, s14, 0x1de0000
	s_mul_i32 s14, s14, 0x1580000
	v_writelane_b32 v255, s17, 8
	v_writelane_b32 v255, s14, 9
	s_mov_b32 s13, s97
	s_nop 0
	v_writelane_b32 v255, s15, 10
	s_add_u32 s14, s8, 0x23a80000
	s_addc_u32 s15, s9, 0
	v_writelane_b32 v255, s14, 11
	s_add_u32 s8, s8, 0x1a700000
	s_addc_u32 s9, s9, 0
	v_writelane_b32 v255, s15, 12
	v_writelane_b32 v255, s8, 13
	s_lshl_b64 s[4:5], s[4:5], 2
	s_lshl_b32 s7, s3, 4
	v_writelane_b32 v255, s9, 14
	v_writelane_b32 v255, s4, 15
	s_add_i32 s72, s7, 0xc00
	s_lshl_b32 s7, s3, 1
	v_writelane_b32 v255, s5, 16
	s_lshl_b64 s[4:5], s[10:11], 2
	v_writelane_b32 v255, s4, 17
	s_lshl_b32 s66, s3, 6
	s_lshl_b32 s67, s6, 9
	v_writelane_b32 v255, s5, 18
	s_lshl_b64 s[4:5], s[12:13], 2
	v_writelane_b32 v255, s4, 19
	s_lshl_b32 s68, s3, 5
	s_lshl_b32 s69, s6, 8
	v_writelane_b32 v255, s5, 20
	v_writelane_b32 v255, s80, 21
	s_lshl_b32 s70, s3, 2
	s_lshl_b32 s71, s6, 5
	v_writelane_b32 v255, s81, 22
	v_writelane_b32 v255, s82, 23
	s_lshl_b32 s73, s6, 7
	s_add_i32 s74, s7, 0x13500
	s_lshl_b32 s75, s6, 4
	v_writelane_b32 v255, s83, 24
	s_branch .Lcvp0c_31

; #define LAS __attribute__((address_space(3)))
; __global__ void __launch_bounds__(NWAVES * 64, 2) mk_fwd(Args args) {
;     ...
;             LAS float* scr = (LAS float*)(lds + RING_OFF + wave * 16640);   static_assert(8 * 16640 <= LDSCTL_OFF, "converter scratch below the LDS control words");
;             constexpr int I_UP = (D / 64) * (NUP / 64), I_DN = (DFF / 64) * (D / 64), I_IN = (D / 64) * (DINP / 64), I_GLU = 16 * 16, I_L = 4 * 16, I_V1 = 16 * 4, I_V2 = 4 * 16,
;                           I_BS5 = 16 * 32, I_BAT = 8 * 32, I_BRW = 16 * 32, I_OUT = 32 * 32;
;             constexpr int NITEMS = 2 * I_UP + 2 * I_DN + I_IN + I_GLU + 3 * I_L + I_V1 + I_V2 + I_BS5 + I_BAT + I_BRW + I_OUT;
;             const int lv = l > 0 ? l - 1 : 0;
;     ...
;             for (int it = gw; it < NITEMS; it += NGW) {
;                 ConvItem ca; CONV_DESC(ca, it);
;                 float va[64];
;                 conv_load(ca, lane, va);
;                 conv_store(ca, scr, lane, va);
;             }
.LBB0_142:
	v_readlane_b32 s99, v254, 35
	v_readlane_b32 s98, v254, 38
	s_nop 3
	s_cmp_lt_u32 s99, 96
	s_cbranch_scc1 .Lcvskip_p1
	v_mov_b32_e32 v250, v254
	v_mov_b32_e32 v251, v255
	v_writelane_b32 v252, s0, 0
	s_nop 0
	v_writelane_b32 v252, s1, 1
	s_nop 0
	v_writelane_b32 v252, s2, 2
	s_nop 0
	v_writelane_b32 v252, s3, 3
	s_nop 0
	v_writelane_b32 v252, s4, 4
	s_nop 0
	v_writelane_b32 v252, s5, 5
	s_nop 0
	v_writelane_b32 v252, s6, 6
	s_nop 0
	v_writelane_b32 v252, s7, 7
	s_nop 0
	v_writelane_b32 v252, s8, 8
	s_nop 0
	v_writelane_b32 v252, s9, 9
	s_nop 0
	v_writelane_b32 v252, s10, 10
	s_nop 0
	v_writelane_b32 v252, s11, 11
	s_nop 0
	v_writelane_b32 v252, s12, 12
	s_nop 0
	v_writelane_b32 v252, s13, 13
	s_nop 0
	v_writelane_b32 v252, s14, 14
	s_nop 0
	v_writelane_b32 v252, s15, 15
	s_nop 0
	v_writelane_b32 v252, s16, 16
	s_nop 0
	v_writelane_b32 v252, s17, 17
	s_nop 0
	v_writelane_b32 v252, s18, 18
	s_nop 0
	v_writelane_b32 v252, s19, 19
	s_nop 0
	v_writelane_b32 v252, s20, 20
	s_nop 0
	v_writelane_b32 v252, s21, 21
	s_nop 0
	v_writelane_b32 v252, s22, 22
	s_nop 0
	v_writelane_b32 v252, s23, 23
	s_nop 0
	v_writelane_b32 v252, s24, 24
	s_nop 0
	v_writelane_b32 v252, s25, 25
	s_nop 0
	v_writelane_b32 v252, s26, 26
	s_nop 0
	v_writelane_b32 v252, s27, 27
	s_nop 0
	v_writelane_b32 v252, s28, 28
	s_nop 0
	v_writelane_b32 v252, s29, 29
	s_nop 0
	v_writelane_b32 v252, s30, 30
	s_nop 0
	v_writelane_b32 v252, s31, 31
	s_nop 0
	v_writelane_b32 v252, s32, 32
	s_nop 0
	v_writelane_b32 v252, s33, 33
	s_nop 0
	v_writelane_b32 v252, s34, 34
	s_nop 0
	v_writelane_b32 v252, s35, 35
	s_nop 0
	v_writelane_b32 v252, s36, 36
	s_nop 0
	v_writelane_b32 v252, s37, 37
	s_nop 0
	v_writelane_b32 v252, s38, 38
	s_nop 0
	v_writelane_b32 v252, s39, 39
	s_nop 0
	v_writelane_b32 v252, s40, 40
	s_nop 0
	v_writelane_b32 v252, s41, 41
	s_nop 0
	v_writelane_b32 v252, s42, 42
	s_nop 0
	v_writelane_b32 v252, s43, 43
	s_nop 0
	v_writelane_b32 v252, s44, 44
	s_nop 0
	v_writelane_b32 v252, s45, 45
	s_nop 0
	v_writelane_b32 v252, s46, 46
	s_nop 0
	v_writelane_b32 v252, s47, 47
	s_nop 0
	v_writelane_b32 v252, s48, 48
	s_nop 0
	v_writelane_b32 v252, s49, 49
	s_nop 0
	v_writelane_b32 v252, s50, 50
	s_nop 0
	v_writelane_b32 v252, s51, 51
	s_nop 0
	v_writelane_b32 v252, s52, 52
	s_nop 0
	v_writelane_b32 v252, s53, 53
	s_nop 0
	v_writelane_b32 v252, s54, 54
	s_nop 0
	v_writelane_b32 v252, s55, 55
	s_nop 0
	v_writelane_b32 v252, s56, 56
	s_nop 0
	v_writelane_b32 v252, s57, 57
	s_nop 0
	v_writelane_b32 v252, s58, 58
	s_nop 0
	v_writelane_b32 v252, s59, 59
	s_nop 0
	v_writelane_b32 v252, s60, 60
	s_nop 0
	v_writelane_b32 v252, s61, 61
	s_nop 0
	v_writelane_b32 v252, s62, 62
	s_nop 0
	v_writelane_b32 v252, s63, 63
	s_nop 0
	v_writelane_b32 v253, s64, 0
	s_nop 0
	v_writelane_b32 v253, s65, 1
	s_nop 0
	v_writelane_b32 v253, s66, 2
	s_nop 0
	v_writelane_b32 v253, s67, 3
	s_nop 0
	v_writelane_b32 v253, s68, 4
	s_nop 0
	v_writelane_b32 v253, s69, 5
	s_nop 0
	v_writelane_b32 v253, s70, 6
	s_nop 0
	v_writelane_b32 v253, s71, 7
	s_nop 0
	v_writelane_b32 v253, s72, 8
	s_nop 0
	v_writelane_b32 v253, s73, 9
	s_nop 0
	v_writelane_b32 v253, s74, 10
	s_nop 0
	v_writelane_b32 v253, s75, 11
	s_nop 0
	v_writelane_b32 v253, s76, 12
	s_nop 0
	v_writelane_b32 v253, s77, 13
	s_nop 0
	v_writelane_b32 v253, s78, 14
	s_nop 0
	v_writelane_b32 v253, s79, 15
	s_nop 0
	v_writelane_b32 v253, s80, 16
	s_nop 0
	v_writelane_b32 v253, s81, 17
	s_nop 0
	v_writelane_b32 v253, s82, 18
	s_nop 0
	v_writelane_b32 v253, s83, 19
	s_nop 0
	v_writelane_b32 v253, s84, 20
	s_nop 0
	v_writelane_b32 v253, s85, 21
	s_nop 0
	v_writelane_b32 v253, s86, 22
	s_nop 0
	v_writelane_b32 v253, s87, 23
	s_nop 0
	v_writelane_b32 v253, s88, 24
	s_nop 0
	v_writelane_b32 v253, s89, 25
	s_nop 0
	v_writelane_b32 v253, s90, 26
	s_nop 0
	v_writelane_b32 v253, s91, 27
	s_nop 0
	v_writelane_b32 v253, s92, 28
	s_nop 0
	v_writelane_b32 v253, s93, 29
	s_nop 0
	v_writelane_b32 v253, s94, 30
	s_nop 0
	v_writelane_b32 v253, s95, 31
	s_nop 0
	v_writelane_b32 v253, s96, 32
	s_nop 0
	v_writelane_b32 v253, s97, 33
	s_nop 0
	v_writelane_b32 v253, vcc_lo, 34
	s_nop 0
	v_writelane_b32 v253, vcc_hi, 35
	s_nop 1
	v_readlane_b32 s84, v254, 35
	s_nop 3
	v_readlane_b32 s0, v254, 8
	v_readlane_b32 s4, v254, 10
	v_readlane_b32 s1, v254, 9
	v_mbcnt_lo_u32_b32 v11, -1, 0
	v_mbcnt_hi_u32_b32 v11, -1, v11
	s_load_dword s6, s[0:1], 0x0
	s_mov_b32 s3, s84
	s_waitcnt lgkmcnt(0)
	s_movk_i32 s6, 160
	s_lshl_b32 s3, s3, 3
	v_readlane_b32 s0, v254, 0
	s_add_i32 s3, s3, s4
	s_add_i32 s3, s3, 0x1280
	v_readlane_b32 s1, v254, 1
	s_cmpk_gt_i32 s3, 11007
	s_cbranch_scc1 .Lcvp10_ret
; #define LAS __attribute__((address_space(3)))
; __global__ void __launch_bounds__(NWAVES * 64, 2) mk_fwd(Args args) {
;     ...
;             LAS float* scr = (LAS float*)(lds + RING_OFF + wave * 16640);   static_assert(8 * 16640 <= LDSCTL_OFF, "converter scratch below the LDS control words");
;             constexpr int I_UP = (D / 64) * (NUP / 64), I_DN = (DFF / 64) * (D / 64), I_IN = (D / 64) * (DINP / 64), I_GLU = 16 * 16, I_L = 4 * 16, I_V1 = 16 * 4, I_V2 = 4 * 16,
;                           I_BS5 = 16 * 32, I_BAT = 8 * 32, I_BRW = 16 * 32, I_OUT = 32 * 32;
;             constexpr int NITEMS = 2 * I_UP + 2 * I_DN + I_IN + I_GLU + 3 * I_L + I_V1 + I_V2 + I_BS5 + I_BAT + I_BRW + I_OUT;
;             const int lv = l > 0 ? l - 1 : 0;
;     ...
;             for (int it = gw; it < NITEMS; it += NGW) {
;                 ConvItem ca; CONV_DESC(ca, it);
;                 float va[64];
;                 conv_load(ca, lane, va);
;                 conv_store(ca, scr, lane, va);
;             }
	s_load_dwordx2 s[8:9], s[0:1], 0x138
	v_readlane_b32 s14, v254, 38
	s_mulk_i32 s4, 0x4100
	s_add_i32 s7, s4, 0
	v_sub_u32_e64 v0, s14, 1 clamp
	s_lshl_b32 s33, s6, 3
	v_readfirstlane_b32 s4, v0
	s_lshl_b32 s96, s4, 16
	s_waitcnt lgkmcnt(0)
	s_add_u32 s4, s8, 0x22800000
	s_addc_u32 s5, s9, 0
	v_writelane_b32 v254, s4, 39
	s_mov_b32 s15, s97
	v_and_b32_e32 v0, 7, v11
	v_writelane_b32 v254, s5, 40
	s_add_u32 s4, s8, 0x22780000
	s_addc_u32 s5, s9, 0
	v_writelane_b32 v254, s4, 41
	v_ashrrev_i32_e32 v13, 3, v11
	v_lshlrev_b32_e32 v10, 3, v0
	v_writelane_b32 v254, s5, 42
	s_lshl_b32 s4, s14, 18
	s_add_u32 s10, s8, 0x22700000
	s_addc_u32 s11, s9, 0
	v_writelane_b32 v254, s10, 43
	s_mov_b32 s5, s97
	v_mul_u32_u24_e32 v0, 0x820, v0
	v_writelane_b32 v254, s11, 44
	s_mul_i32 s10, s14, 0x18000
	s_mov_b32 s11, s97
	v_writelane_b32 v254, s10, 45
	v_lshlrev_b32_e32 v1, 2, v13
	v_lshl_add_u32 v12, v11, 2, s7
	v_writelane_b32 v254, s11, 46
	s_add_u32 s10, s8, 0x22680000
	s_addc_u32 s11, s9, 0
	v_writelane_b32 v254, s10, 47
	v_add3_u32 v14, s7, v0, v1
	s_mov_b32 s41, s97
	v_writelane_b32 v254, s11, 48
	s_add_u32 s10, s8, 0x22600000
	s_addc_u32 s11, s9, 0
	v_writelane_b32 v254, s10, 49
	s_nop 1
	v_writelane_b32 v254, s11, 50
	s_lshl_b32 s10, s14, 20
	s_mov_b32 s11, s97
	v_writelane_b32 v254, s10, 51
	s_nop 1
	v_writelane_b32 v254, s11, 52
	s_add_u32 s10, s8, 0x22400000
	s_addc_u32 s11, s9, 0
	v_writelane_b32 v254, s10, 53
	s_nop 1
	v_writelane_b32 v254, s11, 54
	s_lshl_b32 s10, s14, 21
	s_mov_b32 s11, s97
	v_writelane_b32 v254, s10, 55
	s_nop 1
	v_writelane_b32 v254, s11, 56
	s_add_u32 s10, s8, 0x22e80000
	s_addc_u32 s11, s9, 0
	v_writelane_b32 v254, s10, 57
	s_nop 1
	v_writelane_b32 v254, s11, 58
	s_add_u32 s10, s8, 0x27b80000
	s_addc_u32 s11, s9, 0
	v_writelane_b32 v254, s10, 59
	s_nop 1
	v_writelane_b32 v254, s11, 60
	s_add_u32 s10, s8, 0x22880000
	s_addc_u32 s11, s9, 0
	v_writelane_b32 v254, s10, 61
	s_nop 1
	v_writelane_b32 v254, s11, 62
	s_lshl_b32 s10, s14, 22
	s_add_u32 s12, s8, 0x23280000
	s_addc_u32 s13, s9, 0
	v_writelane_b32 v254, s12, 63
	s_mov_b32 s11, s97
	s_nop 0
	v_writelane_b32 v255, s13, 0
	s_mul_i32 s12, s14, 0xac0000
	s_mov_b32 s13, s97
	v_writelane_b32 v255, s12, 1
	s_nop 1
	v_writelane_b32 v255, s13, 2
	s_add_u32 s12, s8, 0x26580000
	s_addc_u32 s13, s9, 0
	v_writelane_b32 v255, s12, 3
	s_nop 1
	v_writelane_b32 v255, s13, 4
	s_add_u32 s12, s8, 0x1d200000
	s_addc_u32 s13, s9, 0
	s_lshl_b32 s40, s14, 11
	v_writelane_b32 v255, s12, 5
	s_add_u32 s16, s8, 0x1e800000
	s_addc_u32 s17, s9, 0
	v_writelane_b32 v255, s13, 6
	v_writelane_b32 v255, s16, 7
	s_mul_i32 s12, s14, 0x1de0000
	s_mul_i32 s14, s14, 0x1580000
	v_writelane_b32 v255, s17, 8
	v_writelane_b32 v255, s14, 9
	s_mov_b32 s13, s97
	s_nop 0
	v_writelane_b32 v255, s15, 10
	s_add_u32 s14, s8, 0x23a80000
	s_addc_u32 s15, s9, 0
	v_writelane_b32 v255, s14, 11
	s_add_u32 s8, s8, 0x1a700000
	s_addc_u32 s9, s9, 0
	v_writelane_b32 v255, s15, 12
	v_writelane_b32 v255, s8, 13
	s_lshl_b64 s[4:5], s[4:5], 2
	s_lshl_b32 s7, s3, 4
	v_writelane_b32 v255, s9, 14
	v_writelane_b32 v255, s4, 15
	s_add_i32 s72, s7, 0xc00
	s_lshl_b32 s7, s3, 1
	v_writelane_b32 v255, s5, 16
	s_lshl_b64 s[4:5], s[10:11], 2
	v_writelane_b32 v255, s4, 17
	s_lshl_b32 s66, s3, 6
	s_lshl_b32 s67, s6, 9
	v_writelane_b32 v255, s5, 18
	s_lshl_b64 s[4:5], s[12:13], 2
	v_writelane_b32 v255, s4, 19
	s_lshl_b32 s68, s3, 5
	s_lshl_b32 s69, s6, 8
	v_writelane_b32 v255, s5, 20
	v_writelane_b32 v255, s80, 21
	s_lshl_b32 s70, s3, 2
	s_lshl_b32 s71, s6, 5
	v_writelane_b32 v255, s81, 22
	v_writelane_b32 v255, s82, 23
	s_lshl_b32 s73, s6, 7
	s_add_i32 s74, s7, 0x13500
	s_lshl_b32 s75, s6, 4
	v_writelane_b32 v255, s83, 24
	s_branch .Lcvp10_31

; #define LAS __attribute__((address_space(3)))
; __global__ void __launch_bounds__(NWAVES * 64, 2) mk_fwd(Args args) {
;     ...
;             LAS float* scr = (LAS float*)(lds + RING_OFF + wave * 16640);   static_assert(8 * 16640 <= LDSCTL_OFF, "converter scratch below the LDS control words");
;             constexpr int I_UP = (D / 64) * (NUP / 64), I_DN = (DFF / 64) * (D / 64), I_IN = (D / 64) * (DINP / 64), I_GLU = 16 * 16, I_L = 4 * 16, I_V1 = 16 * 4, I_V2 = 4 * 16,
;                           I_BS5 = 16 * 32, I_BAT = 8 * 32, I_BRW = 16 * 32, I_OUT = 32 * 32;
;             constexpr int NITEMS = 2 * I_UP + 2 * I_DN + I_IN + I_GLU + 3 * I_L + I_V1 + I_V2 + I_BS5 + I_BAT + I_BRW + I_OUT;
;             const int lv = l > 0 ? l - 1 : 0;
;     ...
;             for (int it = gw; it < NITEMS; it += NGW) {
;                 ConvItem ca; CONV_DESC(ca, it);
;                 float va[64];
;                 conv_load(ca, lane, va);
;                 conv_store(ca, scr, lane, va);
;             }
.Lcvp10_ret:
.Lcvrs_p10:
	v_readlane_b32 s0, v254, 8
	v_readlane_b32 s4, v254, 10
	v_readlane_b32 s1, v254, 9
	v_mbcnt_lo_u32_b32 v11, -1, 0
	v_mbcnt_hi_u32_b32 v11, -1, v11
	s_load_dword s6, s[0:1], 0x0
	s_mov_b32 s3, s84
	s_waitcnt lgkmcnt(0)
	s_movk_i32 s6, 160
	s_lshl_b32 s3, s3, 3
	v_readlane_b32 s0, v254, 0
	s_add_i32 s3, s3, s4
	s_add_i32 s3, s3, 0x5f80
	v_readlane_b32 s1, v254, 1
	s_cmpk_gt_i32 s3, 26495
	s_cbranch_scc1 .Lcvp11_ret
	s_load_dwordx2 s[8:9], s[0:1], 0x138
	v_readlane_b32 s14, v254, 38
	s_mulk_i32 s4, 0x4100
	s_add_i32 s7, s4, 0
	v_sub_u32_e64 v0, s14, 1 clamp
	s_lshl_b32 s33, s6, 3
	v_readfirstlane_b32 s4, v0
	s_lshl_b32 s96, s4, 16
	s_waitcnt lgkmcnt(0)
	s_add_u32 s4, s8, 0x22800000
	s_addc_u32 s5, s9, 0
	v_writelane_b32 v254, s4, 39
	s_mov_b32 s15, s97
	v_and_b32_e32 v0, 7, v11
	v_writelane_b32 v254, s5, 40
	s_add_u32 s4, s8, 0x22780000
	s_addc_u32 s5, s9, 0
	v_writelane_b32 v254, s4, 41
	v_ashrrev_i32_e32 v13, 3, v11
	v_lshlrev_b32_e32 v10, 3, v0
	v_writelane_b32 v254, s5, 42
	s_lshl_b32 s4, s14, 18
	s_add_u32 s10, s8, 0x22700000
	s_addc_u32 s11, s9, 0
	v_writelane_b32 v254, s10, 43
	s_mov_b32 s5, s97
	v_mul_u32_u24_e32 v0, 0x820, v0
	v_writelane_b32 v254, s11, 44
	s_mul_i32 s10, s14, 0x18000
	s_mov_b32 s11, s97
	v_writelane_b32 v254, s10, 45
	v_lshlrev_b32_e32 v1, 2, v13
	v_lshl_add_u32 v12, v11, 2, s7
	v_writelane_b32 v254, s11, 46
	s_add_u32 s10, s8, 0x22680000
	s_addc_u32 s11, s9, 0
	v_writelane_b32 v254, s10, 47
	v_add3_u32 v14, s7, v0, v1
	s_mov_b32 s41, s97
	v_writelane_b32 v254, s11, 48
	s_add_u32 s10, s8, 0x22600000
	s_addc_u32 s11, s9, 0
	v_writelane_b32 v254, s10, 49
	s_nop 1
	v_writelane_b32 v254, s11, 50
	s_lshl_b32 s10, s14, 20
	s_mov_b32 s11, s97
	v_writelane_b32 v254, s10, 51
	s_nop 1
	v_writelane_b32 v254, s11, 52
	s_add_u32 s10, s8, 0x22400000
	s_addc_u32 s11, s9, 0
	v_writelane_b32 v254, s10, 53
	s_nop 1
	v_writelane_b32 v254, s11, 54
	s_lshl_b32 s10, s14, 21
	s_mov_b32 s11, s97
	v_writelane_b32 v254, s10, 55
	s_nop 1
	v_writelane_b32 v254, s11, 56
	s_add_u32 s10, s8, 0x22e80000
	s_addc_u32 s11, s9, 0
	v_writelane_b32 v254, s10, 57
	s_nop 1
	v_writelane_b32 v254, s11, 58
	s_add_u32 s10, s8, 0x27b80000
	s_addc_u32 s11, s9, 0
	v_writelane_b32 v254, s10, 59
	s_nop 1
	v_writelane_b32 v254, s11, 60
	s_add_u32 s10, s8, 0x22880000
	s_addc_u32 s11, s9, 0
	v_writelane_b32 v254, s10, 61
	s_nop 1
	v_writelane_b32 v254, s11, 62
	s_lshl_b32 s10, s14, 22
	s_add_u32 s12, s8, 0x23280000
	s_addc_u32 s13, s9, 0
	v_writelane_b32 v254, s12, 63
	s_mov_b32 s11, s97
	s_nop 0
	v_writelane_b32 v255, s13, 0
	s_mul_i32 s12, s14, 0xac0000
	s_mov_b32 s13, s97
	v_writelane_b32 v255, s12, 1
	s_nop 1
	v_writelane_b32 v255, s13, 2
	s_add_u32 s12, s8, 0x26580000
	s_addc_u32 s13, s9, 0
	v_writelane_b32 v255, s12, 3
	s_nop 1
	v_writelane_b32 v255, s13, 4
	s_add_u32 s12, s8, 0x1d200000
	s_addc_u32 s13, s9, 0
	s_lshl_b32 s40, s14, 11
	v_writelane_b32 v255, s12, 5
	s_add_u32 s16, s8, 0x1e800000
	s_addc_u32 s17, s9, 0
	v_writelane_b32 v255, s13, 6
	v_writelane_b32 v255, s16, 7
	s_mul_i32 s12, s14, 0x1de0000
	s_mul_i32 s14, s14, 0x1580000
	v_writelane_b32 v255, s17, 8
	v_writelane_b32 v255, s14, 9
	s_mov_b32 s13, s97
	s_nop 0
	v_writelane_b32 v255, s15, 10
	s_add_u32 s14, s8, 0x23a80000
	s_addc_u32 s15, s9, 0
	v_writelane_b32 v255, s14, 11
	s_add_u32 s8, s8, 0x1a700000
	s_addc_u32 s9, s9, 0
	v_writelane_b32 v255, s15, 12
	v_writelane_b32 v255, s8, 13
	s_lshl_b64 s[4:5], s[4:5], 2
	s_lshl_b32 s7, s3, 4
	v_writelane_b32 v255, s9, 14
	v_writelane_b32 v255, s4, 15
	s_add_i32 s72, s7, 0xc00
	s_lshl_b32 s7, s3, 1
	v_writelane_b32 v255, s5, 16
	s_lshl_b64 s[4:5], s[10:11], 2
	v_writelane_b32 v255, s4, 17
	s_lshl_b32 s66, s3, 6
	s_lshl_b32 s67, s6, 9
	v_writelane_b32 v255, s5, 18
	s_lshl_b64 s[4:5], s[12:13], 2
	v_writelane_b32 v255, s4, 19
	s_lshl_b32 s68, s3, 5
	s_lshl_b32 s69, s6, 8
	v_writelane_b32 v255, s5, 20
	v_writelane_b32 v255, s80, 21
	s_lshl_b32 s70, s3, 2
	s_lshl_b32 s71, s6, 5
	v_writelane_b32 v255, s81, 22
	v_writelane_b32 v255, s82, 23
	s_lshl_b32 s73, s6, 7
	s_add_i32 s74, s7, 0x13500
	s_lshl_b32 s75, s6, 4
	v_writelane_b32 v255, s83, 24
	s_branch .Lcvp11_31

; __device__ __forceinline__ void conv_load(const ConvItem& ci, int lane, float (&v)[64]) {
;     const bool okc = ci.srcc >= 0 && (ci.srcc + lane) < ci.ncols;
;     const float* base = ci.W + (okc ? ci.srcc + lane : 0);
;     const int kmax = ci.Ksrc - 1;
; #pragma unroll
;     for (int i = 0; i < 64; ++i) { const int k = ci.k0 + i, kk = k < kmax ? k : kmax; v[i] = __builtin_nontemporal_load(base + (size_t)kk * ci.ldw); }
; #pragma unroll
;     for (int i = 0; i < 64; ++i) v[i] = (okc && (ci.k0 + i) < ci.Ksrc) ? v[i] : 0.f;
; }
.Lcvp11_30:
	s_cmp_lt_i32 s58, s76
	s_cselect_b64 s[4:5], -1, 0
	s_and_b64 s[4:5], vcc, s[4:5]
	s_cmp_lt_i32 s64, s76
	s_waitcnt vmcnt(62)
	v_cndmask_b32_e64 v21, 0, v21, s[4:5]
	s_cselect_b64 s[4:5], -1, 0
	s_and_b64 s[4:5], vcc, s[4:5]
	s_cmp_lt_i32 s65, s76
	v_cndmask_b32_e64 v20, 0, v20, s[4:5]
	s_cselect_b64 s[4:5], -1, 0
	s_and_b64 s[4:5], vcc, s[4:5]
	s_cmp_lt_i32 s78, s76
	s_waitcnt vmcnt(61)
	v_cndmask_b32_e64 v19, 0, v19, s[4:5]
	s_cselect_b64 s[4:5], -1, 0
	s_and_b64 s[4:5], vcc, s[4:5]
	s_cmp_lt_i32 s79, s76
	s_waitcnt vmcnt(60)
	v_cndmask_b32_e64 v18, 0, v18, s[4:5]
	s_cselect_b64 s[4:5], -1, 0
	s_and_b64 s[4:5], vcc, s[4:5]
	s_cmp_lt_i32 s80, s76
	s_waitcnt vmcnt(59)
	v_cndmask_b32_e64 v17, 0, v17, s[4:5]
	s_cselect_b64 s[4:5], -1, 0
	s_and_b64 s[4:5], vcc, s[4:5]
	s_cmp_lt_i32 s81, s76
	s_waitcnt vmcnt(58)
	v_cndmask_b32_e64 v16, 0, v16, s[4:5]
	s_cselect_b64 s[4:5], -1, 0
	s_and_b64 s[4:5], vcc, s[4:5]
	s_cmp_lt_i32 s82, s76
	s_waitcnt vmcnt(57)
	v_cndmask_b32_e64 v15, 0, v15, s[4:5]
	s_cselect_b64 s[4:5], -1, 0
	s_and_b64 s[4:5], vcc, s[4:5]
	s_cmp_lt_i32 s83, s76
	s_waitcnt vmcnt(56)
	v_cndmask_b32_e64 v8, 0, v8, s[4:5]
	s_cselect_b64 s[4:5], -1, 0
	s_and_b64 s[4:5], vcc, s[4:5]
	s_cmp_lt_i32 s85, s76
	s_waitcnt vmcnt(55)
	v_cndmask_b32_e64 v29, 0, v29, s[4:5]
	s_cselect_b64 s[4:5], -1, 0
	s_and_b64 s[4:5], vcc, s[4:5]
	s_cmp_lt_i32 s86, s76
	s_waitcnt vmcnt(54)
	v_cndmask_b32_e64 v28, 0, v28, s[4:5]
	s_cselect_b64 s[4:5], -1, 0
	s_and_b64 s[4:5], vcc, s[4:5]
	s_cmp_lt_i32 s87, s76
	s_waitcnt vmcnt(53)
	v_cndmask_b32_e64 v27, 0, v27, s[4:5]
	s_cselect_b64 s[4:5], -1, 0
	s_and_b64 s[4:5], vcc, s[4:5]
	s_cmp_lt_i32 s88, s76
	s_waitcnt vmcnt(52)
	v_cndmask_b32_e64 v26, 0, v26, s[4:5]
	s_cselect_b64 s[4:5], -1, 0
	s_and_b64 s[4:5], vcc, s[4:5]
	s_cmp_lt_i32 s89, s76
	s_waitcnt vmcnt(51)
	v_cndmask_b32_e64 v25, 0, v25, s[4:5]
	s_cselect_b64 s[4:5], -1, 0
	s_and_b64 s[4:5], vcc, s[4:5]
	s_cmp_lt_i32 s90, s76
	s_waitcnt vmcnt(50)
	v_cndmask_b32_e64 v24, 0, v24, s[4:5]
	s_cselect_b64 s[4:5], -1, 0
	s_and_b64 s[4:5], vcc, s[4:5]
	s_cmp_lt_i32 s92, s76
	s_waitcnt vmcnt(49)
	v_cndmask_b32_e64 v23, 0, v23, s[4:5]
	s_cselect_b64 s[4:5], -1, 0
	s_and_b64 s[4:5], vcc, s[4:5]
	s_cmp_lt_i32 s93, s76
	s_waitcnt vmcnt(48)
	v_cndmask_b32_e64 v22, 0, v22, s[4:5]
	s_cselect_b64 s[4:5], -1, 0
	s_and_b64 s[4:5], vcc, s[4:5]
	s_cmp_lt_i32 s94, s76
	s_waitcnt vmcnt(47)
	v_cndmask_b32_e64 v37, 0, v37, s[4:5]
	s_cselect_b64 s[4:5], -1, 0
	s_and_b64 s[4:5], vcc, s[4:5]
	s_cmp_lt_i32 s95, s76
	s_waitcnt vmcnt(46)
	v_cndmask_b32_e64 v36, 0, v36, s[4:5]
	s_cselect_b64 s[4:5], -1, 0
	s_and_b64 s[4:5], vcc, s[4:5]
	s_cmp_lt_i32 s50, s76
	s_waitcnt vmcnt(45)
	v_cndmask_b32_e64 v35, 0, v35, s[4:5]
	s_cselect_b64 s[4:5], -1, 0
	s_and_b64 s[4:5], vcc, s[4:5]
	s_cmp_lt_i32 s51, s76
	s_waitcnt vmcnt(44)
	v_cndmask_b32_e64 v34, 0, v34, s[4:5]
	s_cselect_b64 s[4:5], -1, 0
	s_and_b64 s[4:5], vcc, s[4:5]
	s_cmp_lt_i32 s52, s76
	s_waitcnt vmcnt(43)
	v_cndmask_b32_e64 v33, 0, v33, s[4:5]
	s_cselect_b64 s[4:5], -1, 0
	s_and_b64 s[4:5], vcc, s[4:5]
	s_cmp_lt_i32 s53, s76
	s_waitcnt vmcnt(42)
	v_cndmask_b32_e64 v32, 0, v32, s[4:5]
	s_cselect_b64 s[4:5], -1, 0
	s_and_b64 s[4:5], vcc, s[4:5]
	s_cmp_lt_i32 s6, s76
	s_waitcnt vmcnt(41)
	v_cndmask_b32_e64 v31, 0, v31, s[4:5]
	s_cselect_b64 s[4:5], -1, 0
	s_and_b64 s[4:5], vcc, s[4:5]
	s_cmp_lt_i32 s7, s76
	s_waitcnt vmcnt(40)
	v_cndmask_b32_e64 v30, 0, v30, s[4:5]
	s_cselect_b64 s[4:5], -1, 0
	s_and_b64 s[4:5], vcc, s[4:5]
	s_cmp_lt_i32 s8, s76
	s_waitcnt vmcnt(39)
	v_cndmask_b32_e64 v45, 0, v45, s[4:5]
	s_cselect_b64 s[4:5], -1, 0
	s_and_b64 s[4:5], vcc, s[4:5]
	s_cmp_lt_i32 s9, s76
	s_waitcnt vmcnt(38)
	v_cndmask_b32_e64 v44, 0, v44, s[4:5]
	s_cselect_b64 s[4:5], -1, 0
	s_and_b64 s[4:5], vcc, s[4:5]
	s_cmp_lt_i32 s10, s76
	s_waitcnt vmcnt(37)
	v_cndmask_b32_e64 v43, 0, v43, s[4:5]
	s_cselect_b64 s[4:5], -1, 0
	s_and_b64 s[4:5], vcc, s[4:5]
	s_cmp_lt_i32 s11, s76
	s_waitcnt vmcnt(36)
	v_cndmask_b32_e64 v42, 0, v42, s[4:5]
	s_cselect_b64 s[4:5], -1, 0
	s_and_b64 s[4:5], vcc, s[4:5]
	s_cmp_lt_i32 s14, s76
	s_waitcnt vmcnt(35)
	v_cndmask_b32_e64 v41, 0, v41, s[4:5]
	s_cselect_b64 s[4:5], -1, 0
	s_and_b64 s[4:5], vcc, s[4:5]
	s_cmp_lt_i32 s15, s76
	s_waitcnt vmcnt(34)
	v_cndmask_b32_e64 v40, 0, v40, s[4:5]
	s_cselect_b64 s[4:5], -1, 0
	s_and_b64 s[4:5], vcc, s[4:5]
	s_cmp_lt_i32 s16, s76
	s_waitcnt vmcnt(33)
	v_cndmask_b32_e64 v39, 0, v39, s[4:5]
	s_cselect_b64 s[4:5], -1, 0
	s_and_b64 s[4:5], vcc, s[4:5]
	s_cmp_lt_i32 s17, s76
	s_waitcnt vmcnt(32)
	v_cndmask_b32_e64 v38, 0, v38, s[4:5]
	s_cselect_b64 s[4:5], -1, 0
	s_and_b64 s[4:5], vcc, s[4:5]
	s_cmp_lt_i32 s12, s76
	s_waitcnt vmcnt(31)
	v_cndmask_b32_e64 v53, 0, v53, s[4:5]
	s_cselect_b64 s[4:5], -1, 0
	s_and_b64 s[4:5], vcc, s[4:5]
	s_cmp_lt_i32 s13, s76
	s_waitcnt vmcnt(30)
	v_cndmask_b32_e64 v52, 0, v52, s[4:5]
	s_cselect_b64 s[4:5], -1, 0
	s_and_b64 s[4:5], vcc, s[4:5]
	s_cmp_lt_i32 s20, s76
	s_waitcnt vmcnt(29)
	v_cndmask_b32_e64 v51, 0, v51, s[4:5]
	s_cselect_b64 s[4:5], -1, 0
	s_and_b64 s[4:5], vcc, s[4:5]
	s_cmp_lt_i32 s21, s76
	s_waitcnt vmcnt(28)
	v_cndmask_b32_e64 v50, 0, v50, s[4:5]
	s_cselect_b64 s[4:5], -1, 0
	s_and_b64 s[4:5], vcc, s[4:5]
	s_cmp_lt_i32 s24, s76
	s_waitcnt vmcnt(27)
	v_cndmask_b32_e64 v49, 0, v49, s[4:5]
	s_cselect_b64 s[4:5], -1, 0
	s_and_b64 s[4:5], vcc, s[4:5]
	s_cmp_lt_i32 s25, s76
	s_waitcnt vmcnt(26)
	v_cndmask_b32_e64 v48, 0, v48, s[4:5]
	s_cselect_b64 s[4:5], -1, 0
	s_and_b64 s[4:5], vcc, s[4:5]
	s_cmp_lt_i32 s26, s76
	s_waitcnt vmcnt(25)
	v_cndmask_b32_e64 v47, 0, v47, s[4:5]
	s_cselect_b64 s[4:5], -1, 0
	s_and_b64 s[4:5], vcc, s[4:5]
	s_cmp_lt_i32 s27, s76
	s_waitcnt vmcnt(24)
; #define LAS __attribute__((address_space(3)))
; #define LDS_WAIT() asm volatile("s_waitcnt lgkmcnt(0)" ::: "memory")
; __device__ __forceinline__ void conv_load(const ConvItem& ci, int lane, float (&v)[64]) {
;     ...
;     for (int i = 0; i < 64; ++i) v[i] = (okc && (ci.k0 + i) < ci.Ksrc) ? v[i] : 0.f;
; }
; __device__ __forceinline__ void conv_store(const ConvItem& ci, LAS float* scr, int lane, const float (&v)[64]) {
;     const int c = lane & 7;
;     f32x4 s0 = {1.f, 1.f, 1.f, 1.f}, s1 = s0;
;     if (ci.ks) { const int kb = ci.k0 + 8 * c < ci.Ksrc - 8 ? ci.k0 + 8 * c : ci.Ksrc - 8; s0 = *(const f32x4*)(ci.ks + kb); s1 = *(const f32x4*)(ci.ks + kb + 4); }
; #pragma unroll
;     for (int i = 0; i < 64; ++i) scr[i * 65 + lane] = v[i];
;     LDS_WAIT(); asm volatile("" ::: "memory");
; #pragma unroll
;     for (int j = 0; j < 8; ++j) { const int n = (lane >> 3) + 8 * j; const LAS float* s = scr + (8 * c) * 65 + n;
	v_cndmask_b32_e64 v46, 0, v46, s[4:5]
	s_cselect_b64 s[4:5], -1, 0
	s_and_b64 s[4:5], vcc, s[4:5]
	s_cmp_lt_i32 s18, s76
	s_waitcnt vmcnt(23)
	v_cndmask_b32_e64 v61, 0, v61, s[4:5]
	s_cselect_b64 s[4:5], -1, 0
	s_and_b64 s[4:5], vcc, s[4:5]
	s_cmp_lt_i32 s19, s76
	s_waitcnt vmcnt(22)
	v_cndmask_b32_e64 v60, 0, v60, s[4:5]
	s_cselect_b64 s[4:5], -1, 0
	s_and_b64 s[4:5], vcc, s[4:5]
	s_cmp_lt_i32 s28, s76
	s_waitcnt vmcnt(21)
	v_cndmask_b32_e64 v59, 0, v59, s[4:5]
	s_cselect_b64 s[4:5], -1, 0
	s_and_b64 s[4:5], vcc, s[4:5]
	s_cmp_lt_i32 s29, s76
	s_waitcnt vmcnt(20)
	v_cndmask_b32_e64 v58, 0, v58, s[4:5]
	s_cselect_b64 s[4:5], -1, 0
	s_and_b64 s[4:5], vcc, s[4:5]
	s_cmp_lt_i32 s22, s76
	s_waitcnt vmcnt(19)
	v_cndmask_b32_e64 v57, 0, v57, s[4:5]
	s_cselect_b64 s[4:5], -1, 0
	s_and_b64 s[4:5], vcc, s[4:5]
	s_cmp_lt_i32 s23, s76
	s_waitcnt vmcnt(18)
	v_cndmask_b32_e64 v56, 0, v56, s[4:5]
	s_cselect_b64 s[4:5], -1, 0
	s_and_b64 s[4:5], vcc, s[4:5]
	s_cmp_lt_i32 s30, s76
	s_waitcnt vmcnt(17)
	v_cndmask_b32_e64 v55, 0, v55, s[4:5]
	s_cselect_b64 s[4:5], -1, 0
	s_and_b64 s[4:5], vcc, s[4:5]
	s_cmp_lt_i32 s31, s76
	s_waitcnt vmcnt(16)
	v_cndmask_b32_e64 v54, 0, v54, s[4:5]
	s_cselect_b64 s[4:5], -1, 0
	s_and_b64 s[4:5], vcc, s[4:5]
	s_cmp_lt_i32 s36, s76
	s_waitcnt vmcnt(15)
	v_cndmask_b32_e64 v70, 0, v70, s[4:5]
	s_cselect_b64 s[4:5], -1, 0
	s_and_b64 s[4:5], vcc, s[4:5]
	s_cmp_lt_i32 s37, s76
	s_waitcnt vmcnt(14)
	v_cndmask_b32_e64 v69, 0, v69, s[4:5]
	s_cselect_b64 s[4:5], -1, 0
	s_and_b64 s[4:5], vcc, s[4:5]
	s_cmp_lt_i32 s38, s76
	s_waitcnt vmcnt(13)
	v_cndmask_b32_e64 v68, 0, v68, s[4:5]
	s_cselect_b64 s[4:5], -1, 0
	s_and_b64 s[4:5], vcc, s[4:5]
	s_cmp_lt_i32 s39, s76
	s_waitcnt vmcnt(12)
	v_cndmask_b32_e64 v67, 0, v67, s[4:5]
	s_cselect_b64 s[4:5], -1, 0
	s_and_b64 s[4:5], vcc, s[4:5]
	s_cmp_lt_i32 s34, s76
	s_waitcnt vmcnt(11)
	v_cndmask_b32_e64 v66, 0, v66, s[4:5]
	s_cselect_b64 s[4:5], -1, 0
	s_and_b64 s[4:5], vcc, s[4:5]
	s_cmp_lt_i32 s35, s76
	s_waitcnt vmcnt(10)
	v_cndmask_b32_e64 v64, 0, v64, s[4:5]
	s_cselect_b64 s[4:5], -1, 0
	s_and_b64 s[4:5], vcc, s[4:5]
	s_cmp_lt_i32 s42, s76
	s_waitcnt vmcnt(9)
	v_cndmask_b32_e64 v63, 0, v63, s[4:5]
	s_cselect_b64 s[4:5], -1, 0
	s_and_b64 s[4:5], vcc, s[4:5]
	s_cmp_lt_i32 s43, s76
	s_waitcnt vmcnt(8)
	v_cndmask_b32_e64 v62, 0, v62, s[4:5]
	s_cselect_b64 s[4:5], -1, 0
	s_and_b64 s[4:5], vcc, s[4:5]
	s_cmp_lt_i32 s54, s76
	s_waitcnt vmcnt(7)
	v_cndmask_b32_e64 v65, 0, v65, s[4:5]
	s_cselect_b64 s[4:5], -1, 0
	s_and_b64 s[4:5], vcc, s[4:5]
	s_cmp_lt_i32 s55, s76
	s_waitcnt vmcnt(6)
	v_cndmask_b32_e64 v74, 0, v74, s[4:5]
	s_cselect_b64 s[4:5], -1, 0
	s_and_b64 s[4:5], vcc, s[4:5]
	s_cmp_lt_i32 s46, s76
	ds_write2_b32 v12, v21, v20 offset1:65
	ds_write2_b32 v12, v19, v18 offset0:130 offset1:195
	v_add_u32_e32 v18, 0x400, v12
	s_waitcnt vmcnt(5)
	v_cndmask_b32_e64 v73, 0, v73, s[4:5]
	s_cselect_b64 s[4:5], -1, 0
	ds_write2_b32 v18, v17, v16 offset0:4 offset1:69
	ds_write2_b32 v18, v15, v8 offset0:134 offset1:199
	v_add_u32_e32 v8, 0x800, v12
	s_and_b64 s[4:5], vcc, s[4:5]
	ds_write2_b32 v8, v29, v28 offset0:8 offset1:73
	ds_write2_b32 v8, v27, v26 offset0:138 offset1:203
	v_add_u32_e32 v8, 0xc00, v12
	s_cmp_lt_i32 s47, s76
	ds_write2_b32 v8, v25, v24 offset0:12 offset1:77
	ds_write2_b32 v8, v23, v22 offset0:142 offset1:207
	v_add_u32_e32 v8, 0x1000, v12
	s_waitcnt vmcnt(4)
	v_cndmask_b32_e64 v72, 0, v72, s[4:5]
	s_cselect_b64 s[4:5], -1, 0
	ds_write2_b32 v8, v37, v36 offset0:16 offset1:81
	ds_write2_b32 v8, v35, v34 offset0:146 offset1:211
	v_add_u32_e32 v8, 0x1400, v12
	s_and_b64 s[4:5], vcc, s[4:5]
	ds_write2_b32 v8, v33, v32 offset0:20 offset1:85
	ds_write2_b32 v8, v31, v30 offset0:150 offset1:215
	v_add_u32_e32 v8, 0x1800, v12
	s_cmp_lt_i32 s48, s76
	ds_write2_b32 v8, v45, v44 offset0:24 offset1:89
	ds_write2_b32 v8, v43, v42 offset0:154 offset1:219
	v_add_u32_e32 v8, 0x1c00, v12
	s_waitcnt vmcnt(3)
	v_cndmask_b32_e64 v71, 0, v71, s[4:5]
	s_cselect_b64 s[4:5], -1, 0
	ds_write2_b32 v8, v41, v40 offset0:28 offset1:93
	ds_write2_b32 v8, v39, v38 offset0:158 offset1:223
	v_add_u32_e32 v8, 0x2000, v12
	s_and_b64 s[4:5], vcc, s[4:5]
	ds_write2_b32 v8, v53, v52 offset0:32 offset1:97
	ds_write2_b32 v8, v51, v50 offset0:162 offset1:227
	v_add_u32_e32 v8, 0x2400, v12
	s_cmp_lt_i32 s49, s76
	ds_write2_b32 v8, v49, v48 offset0:36 offset1:101
	ds_write2_b32 v8, v47, v46 offset0:166 offset1:231
	v_add_u32_e32 v8, 0x2800, v12
	s_waitcnt vmcnt(2)
	v_cndmask_b32_e64 v77, 0, v77, s[4:5]
	s_cselect_b64 s[4:5], -1, 0
	ds_write2_b32 v8, v61, v60 offset0:40 offset1:105
	ds_write2_b32 v8, v59, v58 offset0:170 offset1:235
	v_add_u32_e32 v8, 0x2c00, v12
	s_and_b64 s[4:5], vcc, s[4:5]
	ds_write2_b32 v8, v57, v56 offset0:44 offset1:109
	ds_write2_b32 v8, v55, v54 offset0:174 offset1:239
	v_add_u32_e32 v8, 0x3000, v12
	s_cmp_lt_i32 s44, s76
	ds_write2_b32 v8, v70, v69 offset0:48 offset1:113
	ds_write2_b32 v8, v68, v67 offset0:178 offset1:243
	v_add_u32_e32 v8, 0x3400, v12
	s_waitcnt vmcnt(1)
	v_cndmask_b32_e64 v76, 0, v76, s[4:5]
	s_cselect_b64 s[4:5], -1, 0
	ds_write2_b32 v8, v66, v64 offset0:52 offset1:117
	ds_write2_b32 v8, v63, v62 offset0:182 offset1:247
	v_add_u32_e32 v8, 0x3800, v12
	s_and_b64 vcc, vcc, s[4:5]
	ds_write2_b32 v8, v65, v74 offset0:56 offset1:121
	ds_write2_b32 v8, v73, v72 offset0:186 offset1:251
	v_add_u32_e32 v8, 0x3c00, v12
	s_waitcnt vmcnt(0)
	v_cndmask_b32_e32 v75, 0, v75, vcc
	ds_write2_b32 v8, v71, v77 offset0:60 offset1:125
	ds_write2_b32 v8, v76, v75 offset0:190 offset1:255
	s_waitcnt lgkmcnt(0)
	ds_read2_b32 v[16:17], v14 offset1:65
	v_add_u32_e32 v24, s59, v13
	v_mul_lo_u32 v22, s57, v24
	s_ashr_i32 s59, s58, 31
	v_readlane_b32 s76, v254, 31
	s_waitcnt lgkmcnt(0)
; __device__ __forceinline__ unsigned cvt_pk_bf16(float lo, float hi) { unsigned r; asm volatile("v_cvt_pk_bf16_f32 %0, %1, %2" : "=v"(r) : "v"(lo), "v"(hi)); return r; }
; #define LAS __attribute__((address_space(3)))
; #define LDS_WAIT() asm volatile("s_waitcnt lgkmcnt(0)" ::: "memory")
; __device__ __forceinline__ void conv_store(const ConvItem& ci, LAS float* scr, int lane, const float (&v)[64]) {
;     const int c = lane & 7;
;     f32x4 s0 = {1.f, 1.f, 1.f, 1.f}, s1 = s0;
;     if (ci.ks) { const int kb = ci.k0 + 8 * c < ci.Ksrc - 8 ? ci.k0 + 8 * c : ci.Ksrc - 8; s0 = *(const f32x4*)(ci.ks + kb); s1 = *(const f32x4*)(ci.ks + kb + 4); }
; #pragma unroll
;     for (int i = 0; i < 64; ++i) scr[i * 65 + lane] = v[i];
;     LDS_WAIT(); asm volatile("" ::: "memory");
; #pragma unroll
;     for (int j = 0; j < 8; ++j) { const int n = (lane >> 3) + 8 * j; const LAS float* s = scr + (8 * c) * 65 + n;
;         v4u o; o.x = cvt_pk_bf16(s[0 * 65] * s0[0], s[1 * 65] * s0[1]); o.y = cvt_pk_bf16(s[2 * 65] * s0[2], s[3 * 65] * s0[3]); o.z = cvt_pk_bf16(s[4 * 65] * s1[0], s[5 * 65] * s1[1]); o.w = cvt_pk_bf16(s[6 * 65] * s1[2], s[7 * 65] * s1[3]);
;         *(v4u*)(ci.dst + (size_t)(ci.drow0 + n) * ci.ldd + ci.k0 + 8 * c) = o; }
;     LDS_WAIT(); asm volatile("" ::: "memory");
	v_mul_f32_e32 v8, v4, v16
	v_mul_f32_e32 v15, v5, v17
	v_cvt_pk_bf16_f32 v16, v8, v15
	ds_read2_b32 v[18:19], v14 offset0:130 offset1:195
	s_add_i32 s3, s3, s33
	s_add_i32 s66, s66, s67
	s_add_i32 s68, s68, s69
	s_add_i32 s70, s70, s71
	s_waitcnt lgkmcnt(0)
	v_mul_f32_e32 v15, v7, v19
	v_mul_f32_e32 v8, v6, v18
	v_cvt_pk_bf16_f32 v17, v8, v15
	v_add_u32_e32 v15, 0x400, v14
	ds_read2_b32 v[18:19], v15 offset0:4 offset1:69
	s_add_i32 s72, s72, s73
	s_add_i32 s74, s74, s75
	v_readlane_b32 s78, v254, 33
	v_readlane_b32 s79, v254, 34
	s_waitcnt lgkmcnt(0)
	v_mul_f32_e32 v8, v0, v18
	v_mul_f32_e32 v18, v1, v19
	v_cvt_pk_bf16_f32 v18, v8, v18
	ds_read2_b32 v[20:21], v15 offset0:134 offset1:199
	v_readlane_b32 s80, v255, 21
	v_readlane_b32 s77, v254, 32
	s_movk_i32 s78, 0x1580
	v_readlane_b32 s82, v255, 23
	s_waitcnt lgkmcnt(0)
	v_mul_f32_e32 v8, v2, v20
	v_mul_f32_e32 v19, v3, v21
	v_cvt_pk_bf16_f32 v19, v8, v19
	v_ashrrev_i32_e32 v8, 31, v24
	v_mul_lo_u32 v8, s56, v8
	v_mad_u64_u32 v[20:21], s[4:5], s56, v24, 0
	v_add3_u32 v21, v21, v8, v22
	ds_read2_b32 v[22:23], v14 offset0:8 offset1:73
	v_lshl_add_u64 v[20:21], v[20:21], 1, s[60:61]
	s_lshl_b64 s[4:5], s[58:59], 1
	v_lshl_add_u64 v[20:21], v[20:21], 0, s[4:5]
	v_lshlrev_b32_e32 v8, 1, v10
	v_lshl_add_u64 v[20:21], v[20:21], 0, v[8:9]
	global_store_dwordx4 v[20:21], v[16:19], off
	s_cmpk_lt_i32 s3, 26496
	v_readlane_b32 s83, v255, 24
	s_waitcnt lgkmcnt(0)
	v_mul_f32_e32 v16, v4, v22
	v_mul_f32_e32 v17, v5, v23
	v_cvt_pk_bf16_f32 v16, v16, v17
	ds_read2_b32 v[18:19], v14 offset0:138 offset1:203
	s_mov_b32 s79, 0x3f22f983
	s_mov_b32 s85, 0xbfc90fda
	s_brev_b32 s86, 1
	s_movk_i32 s87, 0x1f8
	s_waitcnt lgkmcnt(0)
	v_mul_f32_e32 v17, v6, v18
	v_mul_f32_e32 v18, v7, v19
	v_cvt_pk_bf16_f32 v17, v17, v18
	ds_read2_b32 v[18:19], v15 offset0:12 offset1:77
	s_mov_b64 s[88:89], 0x80
	s_mov_b64 s[92:93], 0x4000
	s_mov_b64 s[94:95], 0x4800
	v_readlane_b32 s81, v255, 22
	s_waitcnt lgkmcnt(0)
	v_mul_f32_e32 v18, v0, v18
	v_mul_f32_e32 v19, v1, v19
	v_cvt_pk_bf16_f32 v18, v18, v19
	ds_read2_b32 v[20:21], v15 offset0:142 offset1:207
	s_waitcnt lgkmcnt(0)
	v_mul_f32_e32 v19, v2, v20
	v_mul_f32_e32 v20, v3, v21
	v_cvt_pk_bf16_f32 v19, v19, v20
	v_add_u32_e32 v20, 8, v24
	v_ashrrev_i32_e32 v21, 31, v20
	v_mul_lo_u32 v22, s56, v21
	v_mul_lo_u32 v23, s57, v20
	v_mad_u64_u32 v[20:21], s[6:7], s56, v20, 0
	v_add3_u32 v21, v21, v22, v23
	ds_read2_b32 v[22:23], v14 offset0:16 offset1:81
	v_lshl_add_u64 v[20:21], v[20:21], 1, s[60:61]
	v_lshl_add_u64 v[20:21], v[20:21], 0, s[4:5]
	v_lshl_add_u64 v[20:21], v[20:21], 0, v[8:9]
	global_store_dwordx4 v[20:21], v[16:19], off
	s_waitcnt lgkmcnt(0)
	s_nop 0
	v_mul_f32_e32 v16, v4, v22
	v_mul_f32_e32 v17, v5, v23
	v_cvt_pk_bf16_f32 v16, v16, v17
	ds_read2_b32 v[18:19], v14 offset0:146 offset1:211
	s_waitcnt lgkmcnt(0)
	v_mul_f32_e32 v17, v6, v18
	v_mul_f32_e32 v18, v7, v19
	v_cvt_pk_bf16_f32 v17, v17, v18
	ds_read2_b32 v[18:19], v15 offset0:20 offset1:85
	s_waitcnt lgkmcnt(0)
	v_mul_f32_e32 v18, v0, v18
	v_mul_f32_e32 v19, v1, v19
	v_cvt_pk_bf16_f32 v18, v18, v19
	ds_read2_b32 v[20:21], v15 offset0:150 offset1:215
	s_waitcnt lgkmcnt(0)
	v_mul_f32_e32 v19, v2, v20
	v_mul_f32_e32 v20, v3, v21
	v_cvt_pk_bf16_f32 v19, v19, v20
	v_add_u32_e32 v20, 16, v24
	v_ashrrev_i32_e32 v21, 31, v20
	v_mul_lo_u32 v22, s56, v21
	v_mul_lo_u32 v23, s57, v20
	v_mad_u64_u32 v[20:21], s[6:7], s56, v20, 0
	v_add3_u32 v21, v21, v22, v23
	ds_read2_b32 v[22:23], v14 offset0:24 offset1:89
	v_lshl_add_u64 v[20:21], v[20:21], 1, s[60:61]
	v_lshl_add_u64 v[20:21], v[20:21], 0, s[4:5]
	v_lshl_add_u64 v[20:21], v[20:21], 0, v[8:9]
	global_store_dwordx4 v[20:21], v[16:19], off
	s_waitcnt lgkmcnt(0)
	s_nop 0
	v_mul_f32_e32 v16, v4, v22
	v_mul_f32_e32 v17, v5, v23
	v_cvt_pk_bf16_f32 v16, v16, v17
	ds_read2_b32 v[18:19], v14 offset0:154 offset1:219
	s_waitcnt lgkmcnt(0)
	v_mul_f32_e32 v17, v6, v18
	v_mul_f32_e32 v18, v7, v19
	v_cvt_pk_bf16_f32 v17, v17, v18
	ds_read2_b32 v[18:19], v15 offset0:28 offset1:93
	s_waitcnt lgkmcnt(0)
	v_mul_f32_e32 v18, v0, v18
	v_mul_f32_e32 v19, v1, v19
	v_cvt_pk_bf16_f32 v18, v18, v19
	ds_read2_b32 v[20:21], v15 offset0:158 offset1:223
	s_waitcnt lgkmcnt(0)
; __device__ __forceinline__ unsigned cvt_pk_bf16(float lo, float hi) { unsigned r; asm volatile("v_cvt_pk_bf16_f32 %0, %1, %2" : "=v"(r) : "v"(lo), "v"(hi)); return r; }
; #define LAS __attribute__((address_space(3)))
; #define LDS_WAIT() asm volatile("s_waitcnt lgkmcnt(0)" ::: "memory")
; __device__ __forceinline__ void conv_store(const ConvItem& ci, LAS float* scr, int lane, const float (&v)[64]) {
;     ...
;     for (int j = 0; j < 8; ++j) { const int n = (lane >> 3) + 8 * j; const LAS float* s = scr + (8 * c) * 65 + n;
;         v4u o; o.x = cvt_pk_bf16(s[0 * 65] * s0[0], s[1 * 65] * s0[1]); o.y = cvt_pk_bf16(s[2 * 65] * s0[2], s[3 * 65] * s0[3]); o.z = cvt_pk_bf16(s[4 * 65] * s1[0], s[5 * 65] * s1[1]); o.w = cvt_pk_bf16(s[6 * 65] * s1[2], s[7 * 65] * s1[3]);
;         *(v4u*)(ci.dst + (size_t)(ci.drow0 + n) * ci.ldd + ci.k0 + 8 * c) = o; }
;     LDS_WAIT(); asm volatile("" ::: "memory");
	v_mul_f32_e32 v19, v2, v20
	v_mul_f32_e32 v20, v3, v21
	v_cvt_pk_bf16_f32 v19, v19, v20
	v_add_u32_e32 v20, 24, v24
	v_ashrrev_i32_e32 v21, 31, v20
	v_mul_lo_u32 v22, s56, v21
	v_mul_lo_u32 v23, s57, v20
	v_mad_u64_u32 v[20:21], s[6:7], s56, v20, 0
	v_add3_u32 v21, v21, v22, v23
	ds_read2_b32 v[22:23], v14 offset0:32 offset1:97
	v_lshl_add_u64 v[20:21], v[20:21], 1, s[60:61]
	v_lshl_add_u64 v[20:21], v[20:21], 0, s[4:5]
	v_lshl_add_u64 v[20:21], v[20:21], 0, v[8:9]
	global_store_dwordx4 v[20:21], v[16:19], off
	s_waitcnt lgkmcnt(0)
	s_nop 0
	v_mul_f32_e32 v16, v4, v22
	v_mul_f32_e32 v17, v5, v23
	v_cvt_pk_bf16_f32 v16, v16, v17
	ds_read2_b32 v[18:19], v14 offset0:162 offset1:227
	s_waitcnt lgkmcnt(0)
	v_mul_f32_e32 v17, v6, v18
	v_mul_f32_e32 v18, v7, v19
	v_cvt_pk_bf16_f32 v17, v17, v18
	ds_read2_b32 v[18:19], v15 offset0:36 offset1:101
	s_waitcnt lgkmcnt(0)
	v_mul_f32_e32 v18, v0, v18
	v_mul_f32_e32 v19, v1, v19
	v_cvt_pk_bf16_f32 v18, v18, v19
	ds_read2_b32 v[20:21], v15 offset0:166 offset1:231
	s_waitcnt lgkmcnt(0)
	v_mul_f32_e32 v19, v2, v20
	v_mul_f32_e32 v20, v3, v21
	v_cvt_pk_bf16_f32 v19, v19, v20
	v_add_u32_e32 v20, 32, v24
	v_ashrrev_i32_e32 v21, 31, v20
	v_mul_lo_u32 v22, s56, v21
	v_mul_lo_u32 v23, s57, v20
	v_mad_u64_u32 v[20:21], s[6:7], s56, v20, 0
	v_add3_u32 v21, v21, v22, v23
	ds_read2_b32 v[22:23], v14 offset0:40 offset1:105
	v_lshl_add_u64 v[20:21], v[20:21], 1, s[60:61]
	v_lshl_add_u64 v[20:21], v[20:21], 0, s[4:5]
	v_lshl_add_u64 v[20:21], v[20:21], 0, v[8:9]
	global_store_dwordx4 v[20:21], v[16:19], off
	s_waitcnt lgkmcnt(0)
	s_nop 0
	v_mul_f32_e32 v16, v4, v22
	v_mul_f32_e32 v17, v5, v23
	v_cvt_pk_bf16_f32 v16, v16, v17
	ds_read2_b32 v[18:19], v14 offset0:170 offset1:235
	s_waitcnt lgkmcnt(0)
	v_mul_f32_e32 v17, v6, v18
	v_mul_f32_e32 v18, v7, v19
	v_cvt_pk_bf16_f32 v17, v17, v18
	ds_read2_b32 v[18:19], v15 offset0:44 offset1:109
	s_waitcnt lgkmcnt(0)
	v_mul_f32_e32 v18, v0, v18
	v_mul_f32_e32 v19, v1, v19
	v_cvt_pk_bf16_f32 v18, v18, v19
	ds_read2_b32 v[20:21], v15 offset0:174 offset1:239
	s_waitcnt lgkmcnt(0)
	v_mul_f32_e32 v19, v2, v20
	v_mul_f32_e32 v20, v3, v21
	v_cvt_pk_bf16_f32 v19, v19, v20
	v_add_u32_e32 v20, 40, v24
	v_ashrrev_i32_e32 v21, 31, v20
	v_mul_lo_u32 v22, s56, v21
	v_mul_lo_u32 v23, s57, v20
	v_mad_u64_u32 v[20:21], s[6:7], s56, v20, 0
	v_add3_u32 v21, v21, v22, v23
	ds_read2_b32 v[22:23], v14 offset0:48 offset1:113
	v_lshl_add_u64 v[20:21], v[20:21], 1, s[60:61]
	v_lshl_add_u64 v[20:21], v[20:21], 0, s[4:5]
	v_lshl_add_u64 v[20:21], v[20:21], 0, v[8:9]
	global_store_dwordx4 v[20:21], v[16:19], off
	s_waitcnt lgkmcnt(0)
	s_nop 0
	v_mul_f32_e32 v16, v4, v22
	v_mul_f32_e32 v17, v5, v23
	v_cvt_pk_bf16_f32 v16, v16, v17
	ds_read2_b32 v[18:19], v14 offset0:178 offset1:243
	s_waitcnt lgkmcnt(0)
	v_mul_f32_e32 v17, v6, v18
	v_mul_f32_e32 v18, v7, v19
	v_cvt_pk_bf16_f32 v17, v17, v18
	ds_read2_b32 v[18:19], v15 offset0:52 offset1:117
	s_waitcnt lgkmcnt(0)
	v_mul_f32_e32 v18, v0, v18
	v_mul_f32_e32 v19, v1, v19
	v_cvt_pk_bf16_f32 v18, v18, v19
	ds_read2_b32 v[20:21], v15 offset0:182 offset1:247
	s_waitcnt lgkmcnt(0)
	v_mul_f32_e32 v19, v2, v20
	v_mul_f32_e32 v20, v3, v21
	v_cvt_pk_bf16_f32 v19, v19, v20
	v_add_u32_e32 v20, 48, v24
	v_ashrrev_i32_e32 v21, 31, v20
	v_mul_lo_u32 v22, s56, v21
	v_mul_lo_u32 v23, s57, v20
	v_mad_u64_u32 v[20:21], s[6:7], s56, v20, 0
	v_add3_u32 v21, v21, v22, v23
	ds_read2_b32 v[22:23], v14 offset0:56 offset1:121
	v_lshl_add_u64 v[20:21], v[20:21], 1, s[60:61]
	v_lshl_add_u64 v[20:21], v[20:21], 0, s[4:5]
	v_lshl_add_u64 v[20:21], v[20:21], 0, v[8:9]
	global_store_dwordx4 v[20:21], v[16:19], off
	s_waitcnt lgkmcnt(0)
	v_mul_f32_e32 v4, v4, v22
	v_mul_f32_e32 v5, v5, v23
	v_cvt_pk_bf16_f32 v4, v4, v5
	ds_read2_b32 v[16:17], v14 offset0:186 offset1:251
	s_waitcnt lgkmcnt(0)
	v_mul_f32_e32 v5, v6, v16
	v_mul_f32_e32 v6, v7, v17
	v_cvt_pk_bf16_f32 v5, v5, v6
	ds_read2_b32 v[6:7], v15 offset0:60 offset1:125
	s_waitcnt lgkmcnt(0)
	v_mul_f32_e32 v0, v0, v6
	v_mul_f32_e32 v1, v1, v7
	v_cvt_pk_bf16_f32 v6, v0, v1
	ds_read2_b32 v[0:1], v15 offset0:190 offset1:255
	s_waitcnt lgkmcnt(0)
	v_mul_f32_e32 v0, v2, v0
	v_mul_f32_e32 v1, v3, v1
	v_cvt_pk_bf16_f32 v7, v0, v1
	v_add_u32_e32 v0, 56, v24
	v_ashrrev_i32_e32 v1, 31, v0
	v_mul_lo_u32 v2, s56, v1
	v_mul_lo_u32 v3, s57, v0
	v_mad_u64_u32 v[0:1], s[6:7], s56, v0, 0
	v_add3_u32 v1, v1, v2, v3
	v_lshl_add_u64 v[0:1], v[0:1], 1, s[60:61]
	v_lshl_add_u64 v[0:1], v[0:1], 0, s[4:5]
	v_lshl_add_u64 v[0:1], v[0:1], 0, v[8:9]
	global_store_dwordx4 v[0:1], v[4:7], off
	s_waitcnt lgkmcnt(0)
	s_cbranch_scc0 .Lcvp11_ret

; __global__ void __launch_bounds__(NWAVES * 64, 2) mk_fwd(Args args) {
;     ...
;             for (int it = gw; it < NITEMS; it += NGW) {
;                 ConvItem ca; CONV_DESC(ca, it);
;                 float va[64];
;                 conv_load(ca, lane, va);
;                 conv_store(ca, scr, lane, va);
;             }
.Lcvp11_ret:
.Lcvrs_p11:
	v_mov_b32_e32 v254, v250
	v_mov_b32_e32 v255, v251
	s_nop 1
	v_readlane_b32 s0, v252, 0
	v_readlane_b32 s1, v252, 1
	v_readlane_b32 s2, v252, 2
	v_readlane_b32 s3, v252, 3
	v_readlane_b32 s4, v252, 4
	v_readlane_b32 s5, v252, 5
	v_readlane_b32 s6, v252, 6
	v_readlane_b32 s7, v252, 7
	v_readlane_b32 s8, v252, 8
	v_readlane_b32 s9, v252, 9
	v_readlane_b32 s10, v252, 10
	v_readlane_b32 s11, v252, 11
	v_readlane_b32 s12, v252, 12
	v_readlane_b32 s13, v252, 13
	v_readlane_b32 s14, v252, 14
	v_readlane_b32 s15, v252, 15
	v_readlane_b32 s16, v252, 16
	v_readlane_b32 s17, v252, 17
	v_readlane_b32 s18, v252, 18
	v_readlane_b32 s19, v252, 19
	v_readlane_b32 s20, v252, 20
	v_readlane_b32 s21, v252, 21
	v_readlane_b32 s22, v252, 22
	v_readlane_b32 s23, v252, 23
	v_readlane_b32 s24, v252, 24
	v_readlane_b32 s25, v252, 25
	v_readlane_b32 s26, v252, 26
	v_readlane_b32 s27, v252, 27
	v_readlane_b32 s28, v252, 28
	v_readlane_b32 s29, v252, 29
	v_readlane_b32 s30, v252, 30
	v_readlane_b32 s31, v252, 31
	v_readlane_b32 s32, v252, 32
	v_readlane_b32 s33, v252, 33
	v_readlane_b32 s34, v252, 34
	v_readlane_b32 s35, v252, 35
	v_readlane_b32 s36, v252, 36
	v_readlane_b32 s37, v252, 37
	v_readlane_b32 s38, v252, 38
	v_readlane_b32 s39, v252, 39
	v_readlane_b32 s40, v252, 40
	v_readlane_b32 s41, v252, 41
	v_readlane_b32 s42, v252, 42
	v_readlane_b32 s43, v252, 43
	v_readlane_b32 s44, v252, 44
	v_readlane_b32 s45, v252, 45
	v_readlane_b32 s46, v252, 46
	v_readlane_b32 s47, v252, 47
	v_readlane_b32 s48, v252, 48
	v_readlane_b32 s49, v252, 49
	v_readlane_b32 s50, v252, 50
	v_readlane_b32 s51, v252, 51
	v_readlane_b32 s52, v252, 52
	v_readlane_b32 s53, v252, 53
	v_readlane_b32 s54, v252, 54
	v_readlane_b32 s55, v252, 55
	v_readlane_b32 s56, v252, 56
	v_readlane_b32 s57, v252, 57
	v_readlane_b32 s58, v252, 58
	v_readlane_b32 s59, v252, 59
	v_readlane_b32 s60, v252, 60
	v_readlane_b32 s61, v252, 61
	v_readlane_b32 s62, v252, 62
	v_readlane_b32 s63, v252, 63
	v_readlane_b32 s64, v253, 0
	v_readlane_b32 s65, v253, 1
	v_readlane_b32 s66, v253, 2
	v_readlane_b32 s67, v253, 3
	v_readlane_b32 s68, v253, 4
	v_readlane_b32 s69, v253, 5
	v_readlane_b32 s70, v253, 6
	v_readlane_b32 s71, v253, 7
	v_readlane_b32 s72, v253, 8
	v_readlane_b32 s73, v253, 9
	v_readlane_b32 s74, v253, 10
	v_readlane_b32 s75, v253, 11
	v_readlane_b32 s76, v253, 12
	v_readlane_b32 s77, v253, 13
	v_readlane_b32 s78, v253, 14
	v_readlane_b32 s79, v253, 15
	v_readlane_b32 s80, v253, 16
	v_readlane_b32 s81, v253, 17
	v_readlane_b32 s82, v253, 18
	v_readlane_b32 s83, v253, 19
	v_readlane_b32 s84, v253, 20
	v_readlane_b32 s85, v253, 21
	v_readlane_b32 s86, v253, 22
	v_readlane_b32 s87, v253, 23
	v_readlane_b32 s88, v253, 24
	v_readlane_b32 s89, v253, 25
	v_readlane_b32 s90, v253, 26
	v_readlane_b32 s91, v253, 27
	v_readlane_b32 s92, v253, 28
	v_readlane_b32 s93, v253, 29
	v_readlane_b32 s94, v253, 30
	v_readlane_b32 s95, v253, 31
	v_readlane_b32 s96, v253, 32
	v_readlane_b32 s97, v253, 33
	v_readlane_b32 vcc_lo, v253, 34
	v_readlane_b32 vcc_hi, v253, 35
	s_nop 4

; #define LAS __attribute__((address_space(3)))
; __global__ void __launch_bounds__(NWAVES * 64, 2) mk_fwd(Args args) {
;     ...
;             LAS float* scr = (LAS float*)(lds + RING_OFF + wave * 16640);   static_assert(8 * 16640 <= LDSCTL_OFF, "converter scratch below the LDS control words");
;             constexpr int I_UP = (D / 64) * (NUP / 64), I_DN = (DFF / 64) * (D / 64), I_IN = (D / 64) * (DINP / 64), I_GLU = 16 * 16, I_L = 4 * 16, I_V1 = 16 * 4, I_V2 = 4 * 16,
;                           I_BS5 = 16 * 32, I_BAT = 8 * 32, I_BRW = 16 * 32, I_OUT = 32 * 32;
;             constexpr int NITEMS = 2 * I_UP + 2 * I_DN + I_IN + I_GLU + 3 * I_L + I_V1 + I_V2 + I_BS5 + I_BAT + I_BRW + I_OUT;
;             const int lv = l > 0 ? l - 1 : 0;
;     ...
;             for (int it = gw; it < NITEMS; it += NGW) {
;                 ConvItem ca; CONV_DESC(ca, it);
;                 float va[64];
;                 conv_load(ca, lane, va);
;                 conv_store(ca, scr, lane, va);
;             }
.LBB0_346:
	v_readlane_b32 s99, v254, 35
	v_readlane_b32 s98, v254, 38
	s_nop 3
	s_cmp_lt_u32 s99, 128
	s_cbranch_scc1 .Lcvskip_p3
	v_mov_b32_e32 v250, v254
	v_mov_b32_e32 v251, v255
	v_writelane_b32 v252, s0, 0
	s_nop 0
	v_writelane_b32 v252, s1, 1
	s_nop 0
	v_writelane_b32 v252, s2, 2
	s_nop 0
	v_writelane_b32 v252, s3, 3
	s_nop 0
	v_writelane_b32 v252, s4, 4
	s_nop 0
	v_writelane_b32 v252, s5, 5
	s_nop 0
	v_writelane_b32 v252, s6, 6
	s_nop 0
	v_writelane_b32 v252, s7, 7
	s_nop 0
	v_writelane_b32 v252, s8, 8
	s_nop 0
	v_writelane_b32 v252, s9, 9
	s_nop 0
	v_writelane_b32 v252, s10, 10
	s_nop 0
	v_writelane_b32 v252, s11, 11
	s_nop 0
	v_writelane_b32 v252, s12, 12
	s_nop 0
	v_writelane_b32 v252, s13, 13
	s_nop 0
	v_writelane_b32 v252, s14, 14
	s_nop 0
	v_writelane_b32 v252, s15, 15
	s_nop 0
	v_writelane_b32 v252, s16, 16
	s_nop 0
	v_writelane_b32 v252, s17, 17
	s_nop 0
	v_writelane_b32 v252, s18, 18
	s_nop 0
	v_writelane_b32 v252, s19, 19
	s_nop 0
	v_writelane_b32 v252, s20, 20
	s_nop 0
	v_writelane_b32 v252, s21, 21
	s_nop 0
	v_writelane_b32 v252, s22, 22
	s_nop 0
	v_writelane_b32 v252, s23, 23
	s_nop 0
	v_writelane_b32 v252, s24, 24
	s_nop 0
	v_writelane_b32 v252, s25, 25
	s_nop 0
	v_writelane_b32 v252, s26, 26
	s_nop 0
	v_writelane_b32 v252, s27, 27
	s_nop 0
	v_writelane_b32 v252, s28, 28
	s_nop 0
	v_writelane_b32 v252, s29, 29
	s_nop 0
	v_writelane_b32 v252, s30, 30
	s_nop 0
	v_writelane_b32 v252, s31, 31
	s_nop 0
	v_writelane_b32 v252, s32, 32
	s_nop 0
	v_writelane_b32 v252, s33, 33
	s_nop 0
	v_writelane_b32 v252, s34, 34
	s_nop 0
	v_writelane_b32 v252, s35, 35
	s_nop 0
	v_writelane_b32 v252, s36, 36
	s_nop 0
	v_writelane_b32 v252, s37, 37
	s_nop 0
	v_writelane_b32 v252, s38, 38
	s_nop 0
	v_writelane_b32 v252, s39, 39
	s_nop 0
	v_writelane_b32 v252, s40, 40
	s_nop 0
	v_writelane_b32 v252, s41, 41
	s_nop 0
	v_writelane_b32 v252, s42, 42
	s_nop 0
	v_writelane_b32 v252, s43, 43
	s_nop 0
	v_writelane_b32 v252, s44, 44
	s_nop 0
	v_writelane_b32 v252, s45, 45
	s_nop 0
	v_writelane_b32 v252, s46, 46
	s_nop 0
	v_writelane_b32 v252, s47, 47
	s_nop 0
	v_writelane_b32 v252, s48, 48
	s_nop 0
	v_writelane_b32 v252, s49, 49
	s_nop 0
	v_writelane_b32 v252, s50, 50
	s_nop 0
	v_writelane_b32 v252, s51, 51
	s_nop 0
	v_writelane_b32 v252, s52, 52
	s_nop 0
	v_writelane_b32 v252, s53, 53
	s_nop 0
	v_writelane_b32 v252, s54, 54
	s_nop 0
	v_writelane_b32 v252, s55, 55
	s_nop 0
	v_writelane_b32 v252, s56, 56
	s_nop 0
	v_writelane_b32 v252, s57, 57
	s_nop 0
	v_writelane_b32 v252, s58, 58
	s_nop 0
	v_writelane_b32 v252, s59, 59
	s_nop 0
	v_writelane_b32 v252, s60, 60
	s_nop 0
	v_writelane_b32 v252, s61, 61
	s_nop 0
	v_writelane_b32 v252, s62, 62
	s_nop 0
	v_writelane_b32 v252, s63, 63
	s_nop 0
	v_writelane_b32 v253, s64, 0
	s_nop 0
	v_writelane_b32 v253, s65, 1
	s_nop 0
	v_writelane_b32 v253, s66, 2
	s_nop 0
	v_writelane_b32 v253, s67, 3
	s_nop 0
	v_writelane_b32 v253, s68, 4
	s_nop 0
	v_writelane_b32 v253, s69, 5
	s_nop 0
	v_writelane_b32 v253, s70, 6
	s_nop 0
	v_writelane_b32 v253, s71, 7
	s_nop 0
	v_writelane_b32 v253, s72, 8
	s_nop 0
	v_writelane_b32 v253, s73, 9
	s_nop 0
	v_writelane_b32 v253, s74, 10
	s_nop 0
	v_writelane_b32 v253, s75, 11
	s_nop 0
	v_writelane_b32 v253, s76, 12
	s_nop 0
	v_writelane_b32 v253, s77, 13
	s_nop 0
	v_writelane_b32 v253, s78, 14
	s_nop 0
	v_writelane_b32 v253, s79, 15
	s_nop 0
	v_writelane_b32 v253, s80, 16
	s_nop 0
	v_writelane_b32 v253, s81, 17
	s_nop 0
	v_writelane_b32 v253, s82, 18
	s_nop 0
	v_writelane_b32 v253, s83, 19
	s_nop 0
	v_writelane_b32 v253, s84, 20
	s_nop 0
	v_writelane_b32 v253, s85, 21
	s_nop 0
	v_writelane_b32 v253, s86, 22
	s_nop 0
	v_writelane_b32 v253, s87, 23
	s_nop 0
	v_writelane_b32 v253, s88, 24
	s_nop 0
	v_writelane_b32 v253, s89, 25
	s_nop 0
	v_writelane_b32 v253, s90, 26
	s_nop 0
	v_writelane_b32 v253, s91, 27
	s_nop 0
	v_writelane_b32 v253, s92, 28
	s_nop 0
	v_writelane_b32 v253, s93, 29
	s_nop 0
	v_writelane_b32 v253, s94, 30
	s_nop 0
	v_writelane_b32 v253, s95, 31
	s_nop 0
	v_writelane_b32 v253, s96, 32
	s_nop 0
	v_writelane_b32 v253, s97, 33
	s_nop 0
	v_writelane_b32 v253, vcc_lo, 34
	s_nop 0
	v_writelane_b32 v253, vcc_hi, 35
	s_nop 1
	v_readlane_b32 s84, v254, 35
	s_nop 3
	v_readlane_b32 s98, v254, 38
	s_nop 3
	s_cmp_gt_u32 s98, 2
	s_cbranch_scc1 .Lcvrs_p30
; #define LAS __attribute__((address_space(3)))
; __global__ void __launch_bounds__(NWAVES * 64, 2) mk_fwd(Args args) {
;     ...
;             LAS float* scr = (LAS float*)(lds + RING_OFF + wave * 16640);   static_assert(8 * 16640 <= LDSCTL_OFF, "converter scratch below the LDS control words");
;             constexpr int I_UP = (D / 64) * (NUP / 64), I_DN = (DFF / 64) * (D / 64), I_IN = (D / 64) * (DINP / 64), I_GLU = 16 * 16, I_L = 4 * 16, I_V1 = 16 * 4, I_V2 = 4 * 16,
;                           I_BS5 = 16 * 32, I_BAT = 8 * 32, I_BRW = 16 * 32, I_OUT = 32 * 32;
;             constexpr int NITEMS = 2 * I_UP + 2 * I_DN + I_IN + I_GLU + 3 * I_L + I_V1 + I_V2 + I_BS5 + I_BAT + I_BRW + I_OUT;
;             const int lv = l > 0 ? l - 1 : 0;
;     ...
;             for (int it = gw; it < NITEMS; it += NGW) {
;                 ConvItem ca; CONV_DESC(ca, it);
;                 float va[64];
;                 conv_load(ca, lane, va);
;                 conv_store(ca, scr, lane, va);
;             }
	v_readlane_b32 s0, v254, 8
	v_readlane_b32 s4, v254, 10
	v_readlane_b32 s1, v254, 9
	v_mbcnt_lo_u32_b32 v11, -1, 0
	v_mbcnt_hi_u32_b32 v11, -1, v11
	s_load_dword s6, s[0:1], 0x0
	s_mov_b32 s3, s84
	s_waitcnt lgkmcnt(0)
	s_movk_i32 s6, 128
	s_lshl_b32 s3, s3, 3
	v_readlane_b32 s0, v254, 0
	s_add_i32 s3, s3, s4
	s_add_i32 s3, s3, 0x4500
	v_readlane_b32 s1, v254, 1
	s_cmpk_gt_i32 s3, 21439
	s_cbranch_scc1 .Lcvp30_ret
	s_load_dwordx2 s[8:9], s[0:1], 0x138
	v_readlane_b32 s14, v254, 38
	s_nop 0
	s_add_i32 s14, s14, 1
	s_mulk_i32 s4, 0x4100
	s_add_i32 s7, s4, 0
	v_sub_u32_e64 v0, s14, 1 clamp
	s_lshl_b32 s33, s6, 3
	v_readfirstlane_b32 s4, v0
	s_lshl_b32 s96, s4, 16
	s_waitcnt lgkmcnt(0)
	s_add_u32 s4, s8, 0x22800000
	s_addc_u32 s5, s9, 0
	v_writelane_b32 v254, s4, 39
	s_mov_b32 s15, s97
	v_and_b32_e32 v0, 7, v11
	v_writelane_b32 v254, s5, 40
	s_add_u32 s4, s8, 0x22780000
	s_addc_u32 s5, s9, 0
	v_writelane_b32 v254, s4, 41
	v_ashrrev_i32_e32 v13, 3, v11
	v_lshlrev_b32_e32 v10, 3, v0
	v_writelane_b32 v254, s5, 42
	s_lshl_b32 s4, s14, 18
	s_add_u32 s10, s8, 0x22700000
	s_addc_u32 s11, s9, 0
	v_writelane_b32 v254, s10, 43
	s_mov_b32 s5, s97
	v_mul_u32_u24_e32 v0, 0x820, v0
	v_writelane_b32 v254, s11, 44
	s_mul_i32 s10, s14, 0x18000
	s_mov_b32 s11, s97
	v_writelane_b32 v254, s10, 45
	v_lshlrev_b32_e32 v1, 2, v13
	v_lshl_add_u32 v12, v11, 2, s7
	v_writelane_b32 v254, s11, 46
	s_add_u32 s10, s8, 0x22680000
	s_addc_u32 s11, s9, 0
	v_writelane_b32 v254, s10, 47
	v_add3_u32 v14, s7, v0, v1
	s_mov_b32 s41, s97
	v_writelane_b32 v254, s11, 48
	s_add_u32 s10, s8, 0x22600000
	s_addc_u32 s11, s9, 0
	v_writelane_b32 v254, s10, 49
	s_nop 1
	v_writelane_b32 v254, s11, 50
	s_lshl_b32 s10, s14, 20
	s_mov_b32 s11, s97
	v_writelane_b32 v254, s10, 51
	s_nop 1
	v_writelane_b32 v254, s11, 52
	s_add_u32 s10, s8, 0x22400000
	s_addc_u32 s11, s9, 0
	v_writelane_b32 v254, s10, 53
	s_nop 1
	v_writelane_b32 v254, s11, 54
	s_lshl_b32 s10, s14, 21
	s_mov_b32 s11, s97
	v_writelane_b32 v254, s10, 55
	s_nop 1
	v_writelane_b32 v254, s11, 56
	s_add_u32 s10, s8, 0x22e80000
	s_addc_u32 s11, s9, 0
	v_writelane_b32 v254, s10, 57
	s_nop 1
	v_writelane_b32 v254, s11, 58
	s_add_u32 s10, s8, 0x27b80000
	s_addc_u32 s11, s9, 0
	v_writelane_b32 v254, s10, 59
	s_nop 1
	v_writelane_b32 v254, s11, 60
	s_add_u32 s10, s8, 0x22880000
	s_addc_u32 s11, s9, 0
	v_writelane_b32 v254, s10, 61
	s_nop 1
	v_writelane_b32 v254, s11, 62
	s_lshl_b32 s10, s14, 22
	s_add_u32 s12, s8, 0x23280000
	s_addc_u32 s13, s9, 0
	v_writelane_b32 v254, s12, 63
	s_mov_b32 s11, s97
	s_nop 0
	v_writelane_b32 v255, s13, 0
	s_mul_i32 s12, s14, 0xac0000
	s_mov_b32 s13, s97
	v_writelane_b32 v255, s12, 1
	s_nop 1
	v_writelane_b32 v255, s13, 2
	s_add_u32 s12, s8, 0x26580000
	s_addc_u32 s13, s9, 0
	v_writelane_b32 v255, s12, 3
	s_nop 1
	v_writelane_b32 v255, s13, 4
	s_add_u32 s12, s8, 0x1d200000
	s_addc_u32 s13, s9, 0
	s_lshl_b32 s40, s14, 11
	v_writelane_b32 v255, s12, 5
	s_add_u32 s16, s8, 0x1e800000
	s_addc_u32 s17, s9, 0
	v_writelane_b32 v255, s13, 6
	v_writelane_b32 v255, s16, 7
	s_mul_i32 s12, s14, 0x1de0000
	s_mul_i32 s14, s14, 0x1580000
	v_writelane_b32 v255, s17, 8
	v_writelane_b32 v255, s14, 9
	s_mov_b32 s13, s97
	s_nop 0
	v_writelane_b32 v255, s15, 10
	s_add_u32 s14, s8, 0x23a80000
	s_addc_u32 s15, s9, 0
	v_writelane_b32 v255, s14, 11
	s_add_u32 s8, s8, 0x1a700000
	s_addc_u32 s9, s9, 0
	v_writelane_b32 v255, s15, 12
	v_writelane_b32 v255, s8, 13
	s_lshl_b64 s[4:5], s[4:5], 2
	s_lshl_b32 s7, s3, 4
	v_writelane_b32 v255, s9, 14
	v_writelane_b32 v255, s4, 15
	s_add_i32 s72, s7, 0xc00
	s_lshl_b32 s7, s3, 1
	v_writelane_b32 v255, s5, 16
	s_lshl_b64 s[4:5], s[10:11], 2
	v_writelane_b32 v255, s4, 17
	s_lshl_b32 s66, s3, 6
	s_lshl_b32 s67, s6, 9
	v_writelane_b32 v255, s5, 18
	s_lshl_b64 s[4:5], s[12:13], 2
	v_writelane_b32 v255, s4, 19
	s_lshl_b32 s68, s3, 5
	s_lshl_b32 s69, s6, 8
	v_writelane_b32 v255, s5, 20
	v_writelane_b32 v255, s80, 21
	s_lshl_b32 s70, s3, 2
	s_lshl_b32 s71, s6, 5
	v_writelane_b32 v255, s81, 22
	v_writelane_b32 v255, s82, 23
	s_lshl_b32 s73, s6, 7
	s_add_i32 s74, s7, 0x13500
	s_lshl_b32 s75, s6, 4
	v_writelane_b32 v255, s83, 24
	s_branch .Lcvp30_31

; #define LAS __attribute__((address_space(3)))
; __global__ void __launch_bounds__(NWAVES * 64, 2) mk_fwd(Args args) {
;     ...
;             LAS float* scr = (LAS float*)(lds + RING_OFF + wave * 16640);   static_assert(8 * 16640 <= LDSCTL_OFF, "converter scratch below the LDS control words");
;             constexpr int I_UP = (D / 64) * (NUP / 64), I_DN = (DFF / 64) * (D / 64), I_IN = (D / 64) * (DINP / 64), I_GLU = 16 * 16, I_L = 4 * 16, I_V1 = 16 * 4, I_V2 = 4 * 16,
;                           I_BS5 = 16 * 32, I_BAT = 8 * 32, I_BRW = 16 * 32, I_OUT = 32 * 32;
;             constexpr int NITEMS = 2 * I_UP + 2 * I_DN + I_IN + I_GLU + 3 * I_L + I_V1 + I_V2 + I_BS5 + I_BAT + I_BRW + I_OUT;
;             const int lv = l > 0 ? l - 1 : 0;
;     ...
;             for (int it = gw; it < NITEMS; it += NGW) {
;                 ConvItem ca; CONV_DESC(ca, it);
;                 float va[64];
;                 conv_load(ca, lane, va);
;                 conv_store(ca, scr, lane, va);
;             }
.Lcvp30_ret:
.Lcvrs_p30:
	v_readlane_b32 s0, v254, 8
	v_readlane_b32 s4, v254, 10
	v_readlane_b32 s1, v254, 9
	v_mbcnt_lo_u32_b32 v11, -1, 0
	v_mbcnt_hi_u32_b32 v11, -1, v11
	s_load_dword s6, s[0:1], 0x0
	s_mov_b32 s3, s84
	s_waitcnt lgkmcnt(0)
	s_movk_i32 s6, 128
	s_lshl_b32 s3, s3, 3
	v_readlane_b32 s0, v254, 0
	s_add_i32 s3, s3, s4
	s_add_i32 s3, s3, 0x4fc0
	v_readlane_b32 s1, v254, 1
	s_cmpk_gt_i32 s3, 25215
	s_cbranch_scc1 .Lcvp31_ret
	s_load_dwordx2 s[8:9], s[0:1], 0x138
	v_readlane_b32 s14, v254, 38
	s_mulk_i32 s4, 0x4100
	s_add_i32 s7, s4, 0
	v_sub_u32_e64 v0, s14, 1 clamp
	s_lshl_b32 s33, s6, 3
	v_readfirstlane_b32 s4, v0
	s_lshl_b32 s96, s4, 16
	s_waitcnt lgkmcnt(0)
	s_add_u32 s4, s8, 0x22800000
	s_addc_u32 s5, s9, 0
	v_writelane_b32 v254, s4, 39
	s_mov_b32 s15, s97
	v_and_b32_e32 v0, 7, v11
	v_writelane_b32 v254, s5, 40
	s_add_u32 s4, s8, 0x22780000
	s_addc_u32 s5, s9, 0
	v_writelane_b32 v254, s4, 41
	v_ashrrev_i32_e32 v13, 3, v11
	v_lshlrev_b32_e32 v10, 3, v0
	v_writelane_b32 v254, s5, 42
	s_lshl_b32 s4, s14, 18
	s_add_u32 s10, s8, 0x22700000
	s_addc_u32 s11, s9, 0
	v_writelane_b32 v254, s10, 43
	s_mov_b32 s5, s97
	v_mul_u32_u24_e32 v0, 0x820, v0
	v_writelane_b32 v254, s11, 44
	s_mul_i32 s10, s14, 0x18000
	s_mov_b32 s11, s97
	v_writelane_b32 v254, s10, 45
	v_lshlrev_b32_e32 v1, 2, v13
	v_lshl_add_u32 v12, v11, 2, s7
	v_writelane_b32 v254, s11, 46
	s_add_u32 s10, s8, 0x22680000
	s_addc_u32 s11, s9, 0
	v_writelane_b32 v254, s10, 47
	v_add3_u32 v14, s7, v0, v1
	s_mov_b32 s41, s97
	v_writelane_b32 v254, s11, 48
	s_add_u32 s10, s8, 0x22600000
	s_addc_u32 s11, s9, 0
	v_writelane_b32 v254, s10, 49
	s_nop 1
	v_writelane_b32 v254, s11, 50
	s_lshl_b32 s10, s14, 20
	s_mov_b32 s11, s97
	v_writelane_b32 v254, s10, 51
	s_nop 1
	v_writelane_b32 v254, s11, 52
	s_add_u32 s10, s8, 0x22400000
	s_addc_u32 s11, s9, 0
	v_writelane_b32 v254, s10, 53
	s_nop 1
	v_writelane_b32 v254, s11, 54
	s_lshl_b32 s10, s14, 21
	s_mov_b32 s11, s97
	v_writelane_b32 v254, s10, 55
	s_nop 1
	v_writelane_b32 v254, s11, 56
	s_add_u32 s10, s8, 0x22e80000
	s_addc_u32 s11, s9, 0
	v_writelane_b32 v254, s10, 57
	s_nop 1
	v_writelane_b32 v254, s11, 58
	s_add_u32 s10, s8, 0x27b80000
	s_addc_u32 s11, s9, 0
	v_writelane_b32 v254, s10, 59
	s_nop 1
	v_writelane_b32 v254, s11, 60
	s_add_u32 s10, s8, 0x22880000
	s_addc_u32 s11, s9, 0
	v_writelane_b32 v254, s10, 61
	s_nop 1
	v_writelane_b32 v254, s11, 62
	s_lshl_b32 s10, s14, 22
	s_add_u32 s12, s8, 0x23280000
	s_addc_u32 s13, s9, 0
	v_writelane_b32 v254, s12, 63
	s_mov_b32 s11, s97
	s_nop 0
	v_writelane_b32 v255, s13, 0
	s_mul_i32 s12, s14, 0xac0000
	s_mov_b32 s13, s97
	v_writelane_b32 v255, s12, 1
	s_nop 1
	v_writelane_b32 v255, s13, 2
	s_add_u32 s12, s8, 0x26580000
	s_addc_u32 s13, s9, 0
	v_writelane_b32 v255, s12, 3
	s_nop 1
	v_writelane_b32 v255, s13, 4
	s_add_u32 s12, s8, 0x1d200000
	s_addc_u32 s13, s9, 0
	s_lshl_b32 s40, s14, 11
	v_writelane_b32 v255, s12, 5
	s_add_u32 s16, s8, 0x1e800000
	s_addc_u32 s17, s9, 0
	v_writelane_b32 v255, s13, 6
	v_writelane_b32 v255, s16, 7
	s_mul_i32 s12, s14, 0x1de0000
	s_mul_i32 s14, s14, 0x1580000
	v_writelane_b32 v255, s17, 8
	v_writelane_b32 v255, s14, 9
	s_mov_b32 s13, s97
	s_nop 0
	v_writelane_b32 v255, s15, 10
	s_add_u32 s14, s8, 0x23a80000
	s_addc_u32 s15, s9, 0
	v_writelane_b32 v255, s14, 11
	s_add_u32 s8, s8, 0x1a700000
	s_addc_u32 s9, s9, 0
	v_writelane_b32 v255, s15, 12
	v_writelane_b32 v255, s8, 13
	s_lshl_b64 s[4:5], s[4:5], 2
	s_lshl_b32 s7, s3, 4
	v_writelane_b32 v255, s9, 14
	v_writelane_b32 v255, s4, 15
	s_add_i32 s72, s7, 0xc00
	s_lshl_b32 s7, s3, 1
	v_writelane_b32 v255, s5, 16
	s_lshl_b64 s[4:5], s[10:11], 2
	v_writelane_b32 v255, s4, 17
	s_lshl_b32 s66, s3, 6
	s_lshl_b32 s67, s6, 9
	v_writelane_b32 v255, s5, 18
	s_lshl_b64 s[4:5], s[12:13], 2
	v_writelane_b32 v255, s4, 19
	s_lshl_b32 s68, s3, 5
	s_lshl_b32 s69, s6, 8
	v_writelane_b32 v255, s5, 20
	v_writelane_b32 v255, s80, 21
	s_lshl_b32 s70, s3, 2
	s_lshl_b32 s71, s6, 5
	v_writelane_b32 v255, s81, 22
	v_writelane_b32 v255, s82, 23
	s_lshl_b32 s73, s6, 7
	s_add_i32 s74, s7, 0x13500
	s_lshl_b32 s75, s6, 4
	v_writelane_b32 v255, s83, 24
	s_branch .Lcvp31_31

; __device__ __forceinline__ void conv_load(const ConvItem& ci, int lane, float (&v)[64]) {
;     const bool okc = ci.srcc >= 0 && (ci.srcc + lane) < ci.ncols;
;     const float* base = ci.W + (okc ? ci.srcc + lane : 0);
;     const int kmax = ci.Ksrc - 1;
; #pragma unroll
;     for (int i = 0; i < 64; ++i) { const int k = ci.k0 + i, kk = k < kmax ? k : kmax; v[i] = __builtin_nontemporal_load(base + (size_t)kk * ci.ldw); }
; #pragma unroll
;     for (int i = 0; i < 64; ++i) v[i] = (okc && (ci.k0 + i) < ci.Ksrc) ? v[i] : 0.f;
; }
.Lcvp31_30:
	s_cmp_lt_i32 s58, s76
	s_cselect_b64 s[4:5], -1, 0
	s_and_b64 s[4:5], vcc, s[4:5]
	s_cmp_lt_i32 s64, s76
	s_waitcnt vmcnt(62)
	v_cndmask_b32_e64 v21, 0, v21, s[4:5]
	s_cselect_b64 s[4:5], -1, 0
	s_and_b64 s[4:5], vcc, s[4:5]
	s_cmp_lt_i32 s65, s76
	v_cndmask_b32_e64 v20, 0, v20, s[4:5]
	s_cselect_b64 s[4:5], -1, 0
	s_and_b64 s[4:5], vcc, s[4:5]
	s_cmp_lt_i32 s78, s76
	s_waitcnt vmcnt(61)
	v_cndmask_b32_e64 v19, 0, v19, s[4:5]
	s_cselect_b64 s[4:5], -1, 0
	s_and_b64 s[4:5], vcc, s[4:5]
	s_cmp_lt_i32 s79, s76
	s_waitcnt vmcnt(60)
	v_cndmask_b32_e64 v18, 0, v18, s[4:5]
	s_cselect_b64 s[4:5], -1, 0
	s_and_b64 s[4:5], vcc, s[4:5]
	s_cmp_lt_i32 s80, s76
	s_waitcnt vmcnt(59)
	v_cndmask_b32_e64 v17, 0, v17, s[4:5]
	s_cselect_b64 s[4:5], -1, 0
	s_and_b64 s[4:5], vcc, s[4:5]
	s_cmp_lt_i32 s81, s76
	s_waitcnt vmcnt(58)
	v_cndmask_b32_e64 v16, 0, v16, s[4:5]
	s_cselect_b64 s[4:5], -1, 0
	s_and_b64 s[4:5], vcc, s[4:5]
	s_cmp_lt_i32 s82, s76
	s_waitcnt vmcnt(57)
	v_cndmask_b32_e64 v15, 0, v15, s[4:5]
	s_cselect_b64 s[4:5], -1, 0
	s_and_b64 s[4:5], vcc, s[4:5]
	s_cmp_lt_i32 s83, s76
	s_waitcnt vmcnt(56)
	v_cndmask_b32_e64 v8, 0, v8, s[4:5]
	s_cselect_b64 s[4:5], -1, 0
	s_and_b64 s[4:5], vcc, s[4:5]
	s_cmp_lt_i32 s85, s76
	s_waitcnt vmcnt(55)
	v_cndmask_b32_e64 v29, 0, v29, s[4:5]
	s_cselect_b64 s[4:5], -1, 0
	s_and_b64 s[4:5], vcc, s[4:5]
	s_cmp_lt_i32 s86, s76
	s_waitcnt vmcnt(54)
	v_cndmask_b32_e64 v28, 0, v28, s[4:5]
	s_cselect_b64 s[4:5], -1, 0
	s_and_b64 s[4:5], vcc, s[4:5]
	s_cmp_lt_i32 s87, s76
	s_waitcnt vmcnt(53)
	v_cndmask_b32_e64 v27, 0, v27, s[4:5]
	s_cselect_b64 s[4:5], -1, 0
	s_and_b64 s[4:5], vcc, s[4:5]
	s_cmp_lt_i32 s88, s76
	s_waitcnt vmcnt(52)
	v_cndmask_b32_e64 v26, 0, v26, s[4:5]
	s_cselect_b64 s[4:5], -1, 0
	s_and_b64 s[4:5], vcc, s[4:5]
	s_cmp_lt_i32 s89, s76
	s_waitcnt vmcnt(51)
	v_cndmask_b32_e64 v25, 0, v25, s[4:5]
	s_cselect_b64 s[4:5], -1, 0
	s_and_b64 s[4:5], vcc, s[4:5]
	s_cmp_lt_i32 s90, s76
	s_waitcnt vmcnt(50)
	v_cndmask_b32_e64 v24, 0, v24, s[4:5]
	s_cselect_b64 s[4:5], -1, 0
	s_and_b64 s[4:5], vcc, s[4:5]
	s_cmp_lt_i32 s92, s76
	s_waitcnt vmcnt(49)
	v_cndmask_b32_e64 v23, 0, v23, s[4:5]
	s_cselect_b64 s[4:5], -1, 0
	s_and_b64 s[4:5], vcc, s[4:5]
	s_cmp_lt_i32 s93, s76
	s_waitcnt vmcnt(48)
	v_cndmask_b32_e64 v22, 0, v22, s[4:5]
	s_cselect_b64 s[4:5], -1, 0
	s_and_b64 s[4:5], vcc, s[4:5]
	s_cmp_lt_i32 s94, s76
	s_waitcnt vmcnt(47)
	v_cndmask_b32_e64 v37, 0, v37, s[4:5]
	s_cselect_b64 s[4:5], -1, 0
	s_and_b64 s[4:5], vcc, s[4:5]
	s_cmp_lt_i32 s95, s76
	s_waitcnt vmcnt(46)
	v_cndmask_b32_e64 v36, 0, v36, s[4:5]
	s_cselect_b64 s[4:5], -1, 0
	s_and_b64 s[4:5], vcc, s[4:5]
	s_cmp_lt_i32 s50, s76
	s_waitcnt vmcnt(45)
	v_cndmask_b32_e64 v35, 0, v35, s[4:5]
	s_cselect_b64 s[4:5], -1, 0
	s_and_b64 s[4:5], vcc, s[4:5]
	s_cmp_lt_i32 s51, s76
	s_waitcnt vmcnt(44)
	v_cndmask_b32_e64 v34, 0, v34, s[4:5]
	s_cselect_b64 s[4:5], -1, 0
	s_and_b64 s[4:5], vcc, s[4:5]
	s_cmp_lt_i32 s52, s76
	s_waitcnt vmcnt(43)
	v_cndmask_b32_e64 v33, 0, v33, s[4:5]
	s_cselect_b64 s[4:5], -1, 0
	s_and_b64 s[4:5], vcc, s[4:5]
	s_cmp_lt_i32 s53, s76
	s_waitcnt vmcnt(42)
	v_cndmask_b32_e64 v32, 0, v32, s[4:5]
	s_cselect_b64 s[4:5], -1, 0
	s_and_b64 s[4:5], vcc, s[4:5]
	s_cmp_lt_i32 s6, s76
	s_waitcnt vmcnt(41)
	v_cndmask_b32_e64 v31, 0, v31, s[4:5]
	s_cselect_b64 s[4:5], -1, 0
	s_and_b64 s[4:5], vcc, s[4:5]
	s_cmp_lt_i32 s7, s76
	s_waitcnt vmcnt(40)
	v_cndmask_b32_e64 v30, 0, v30, s[4:5]
	s_cselect_b64 s[4:5], -1, 0
	s_and_b64 s[4:5], vcc, s[4:5]
	s_cmp_lt_i32 s8, s76
	s_waitcnt vmcnt(39)
	v_cndmask_b32_e64 v45, 0, v45, s[4:5]
	s_cselect_b64 s[4:5], -1, 0
	s_and_b64 s[4:5], vcc, s[4:5]
	s_cmp_lt_i32 s9, s76
	s_waitcnt vmcnt(38)
	v_cndmask_b32_e64 v44, 0, v44, s[4:5]
	s_cselect_b64 s[4:5], -1, 0
	s_and_b64 s[4:5], vcc, s[4:5]
	s_cmp_lt_i32 s10, s76
	s_waitcnt vmcnt(37)
	v_cndmask_b32_e64 v43, 0, v43, s[4:5]
	s_cselect_b64 s[4:5], -1, 0
	s_and_b64 s[4:5], vcc, s[4:5]
	s_cmp_lt_i32 s11, s76
	s_waitcnt vmcnt(36)
	v_cndmask_b32_e64 v42, 0, v42, s[4:5]
	s_cselect_b64 s[4:5], -1, 0
	s_and_b64 s[4:5], vcc, s[4:5]
	s_cmp_lt_i32 s14, s76
	s_waitcnt vmcnt(35)
	v_cndmask_b32_e64 v41, 0, v41, s[4:5]
	s_cselect_b64 s[4:5], -1, 0
	s_and_b64 s[4:5], vcc, s[4:5]
	s_cmp_lt_i32 s15, s76
	s_waitcnt vmcnt(34)
	v_cndmask_b32_e64 v40, 0, v40, s[4:5]
	s_cselect_b64 s[4:5], -1, 0
	s_and_b64 s[4:5], vcc, s[4:5]
	s_cmp_lt_i32 s16, s76
	s_waitcnt vmcnt(33)
	v_cndmask_b32_e64 v39, 0, v39, s[4:5]
	s_cselect_b64 s[4:5], -1, 0
	s_and_b64 s[4:5], vcc, s[4:5]
	s_cmp_lt_i32 s17, s76
	s_waitcnt vmcnt(32)
	v_cndmask_b32_e64 v38, 0, v38, s[4:5]
	s_cselect_b64 s[4:5], -1, 0
	s_and_b64 s[4:5], vcc, s[4:5]
	s_cmp_lt_i32 s12, s76
	s_waitcnt vmcnt(31)
	v_cndmask_b32_e64 v53, 0, v53, s[4:5]
	s_cselect_b64 s[4:5], -1, 0
	s_and_b64 s[4:5], vcc, s[4:5]
	s_cmp_lt_i32 s13, s76
	s_waitcnt vmcnt(30)
	v_cndmask_b32_e64 v52, 0, v52, s[4:5]
	s_cselect_b64 s[4:5], -1, 0
	s_and_b64 s[4:5], vcc, s[4:5]
	s_cmp_lt_i32 s20, s76
	s_waitcnt vmcnt(29)
	v_cndmask_b32_e64 v51, 0, v51, s[4:5]
	s_cselect_b64 s[4:5], -1, 0
	s_and_b64 s[4:5], vcc, s[4:5]
	s_cmp_lt_i32 s21, s76
	s_waitcnt vmcnt(28)
	v_cndmask_b32_e64 v50, 0, v50, s[4:5]
	s_cselect_b64 s[4:5], -1, 0
	s_and_b64 s[4:5], vcc, s[4:5]
	s_cmp_lt_i32 s24, s76
	s_waitcnt vmcnt(27)
	v_cndmask_b32_e64 v49, 0, v49, s[4:5]
	s_cselect_b64 s[4:5], -1, 0
	s_and_b64 s[4:5], vcc, s[4:5]
	s_cmp_lt_i32 s25, s76
	s_waitcnt vmcnt(26)
	v_cndmask_b32_e64 v48, 0, v48, s[4:5]
	s_cselect_b64 s[4:5], -1, 0
	s_and_b64 s[4:5], vcc, s[4:5]
	s_cmp_lt_i32 s26, s76
	s_waitcnt vmcnt(25)
	v_cndmask_b32_e64 v47, 0, v47, s[4:5]
	s_cselect_b64 s[4:5], -1, 0
	s_and_b64 s[4:5], vcc, s[4:5]
	s_cmp_lt_i32 s27, s76
	s_waitcnt vmcnt(24)
; #define LAS __attribute__((address_space(3)))
; #define LDS_WAIT() asm volatile("s_waitcnt lgkmcnt(0)" ::: "memory")
; __device__ __forceinline__ void conv_load(const ConvItem& ci, int lane, float (&v)[64]) {
;     ...
;     for (int i = 0; i < 64; ++i) v[i] = (okc && (ci.k0 + i) < ci.Ksrc) ? v[i] : 0.f;
; }
; __device__ __forceinline__ void conv_store(const ConvItem& ci, LAS float* scr, int lane, const float (&v)[64]) {
;     const int c = lane & 7;
;     f32x4 s0 = {1.f, 1.f, 1.f, 1.f}, s1 = s0;
;     if (ci.ks) { const int kb = ci.k0 + 8 * c < ci.Ksrc - 8 ? ci.k0 + 8 * c : ci.Ksrc - 8; s0 = *(const f32x4*)(ci.ks + kb); s1 = *(const f32x4*)(ci.ks + kb + 4); }
; #pragma unroll
;     for (int i = 0; i < 64; ++i) scr[i * 65 + lane] = v[i];
;     LDS_WAIT(); asm volatile("" ::: "memory");
; #pragma unroll
;     for (int j = 0; j < 8; ++j) { const int n = (lane >> 3) + 8 * j; const LAS float* s = scr + (8 * c) * 65 + n;
	v_cndmask_b32_e64 v46, 0, v46, s[4:5]
	s_cselect_b64 s[4:5], -1, 0
	s_and_b64 s[4:5], vcc, s[4:5]
	s_cmp_lt_i32 s18, s76
	s_waitcnt vmcnt(23)
	v_cndmask_b32_e64 v61, 0, v61, s[4:5]
	s_cselect_b64 s[4:5], -1, 0
	s_and_b64 s[4:5], vcc, s[4:5]
	s_cmp_lt_i32 s19, s76
	s_waitcnt vmcnt(22)
	v_cndmask_b32_e64 v60, 0, v60, s[4:5]
	s_cselect_b64 s[4:5], -1, 0
	s_and_b64 s[4:5], vcc, s[4:5]
	s_cmp_lt_i32 s28, s76
	s_waitcnt vmcnt(21)
	v_cndmask_b32_e64 v59, 0, v59, s[4:5]
	s_cselect_b64 s[4:5], -1, 0
	s_and_b64 s[4:5], vcc, s[4:5]
	s_cmp_lt_i32 s29, s76
	s_waitcnt vmcnt(20)
	v_cndmask_b32_e64 v58, 0, v58, s[4:5]
	s_cselect_b64 s[4:5], -1, 0
	s_and_b64 s[4:5], vcc, s[4:5]
	s_cmp_lt_i32 s22, s76
	s_waitcnt vmcnt(19)
	v_cndmask_b32_e64 v57, 0, v57, s[4:5]
	s_cselect_b64 s[4:5], -1, 0
	s_and_b64 s[4:5], vcc, s[4:5]
	s_cmp_lt_i32 s23, s76
	s_waitcnt vmcnt(18)
	v_cndmask_b32_e64 v56, 0, v56, s[4:5]
	s_cselect_b64 s[4:5], -1, 0
	s_and_b64 s[4:5], vcc, s[4:5]
	s_cmp_lt_i32 s30, s76
	s_waitcnt vmcnt(17)
	v_cndmask_b32_e64 v55, 0, v55, s[4:5]
	s_cselect_b64 s[4:5], -1, 0
	s_and_b64 s[4:5], vcc, s[4:5]
	s_cmp_lt_i32 s31, s76
	s_waitcnt vmcnt(16)
	v_cndmask_b32_e64 v54, 0, v54, s[4:5]
	s_cselect_b64 s[4:5], -1, 0
	s_and_b64 s[4:5], vcc, s[4:5]
	s_cmp_lt_i32 s36, s76
	s_waitcnt vmcnt(15)
	v_cndmask_b32_e64 v70, 0, v70, s[4:5]
	s_cselect_b64 s[4:5], -1, 0
	s_and_b64 s[4:5], vcc, s[4:5]
	s_cmp_lt_i32 s37, s76
	s_waitcnt vmcnt(14)
	v_cndmask_b32_e64 v69, 0, v69, s[4:5]
	s_cselect_b64 s[4:5], -1, 0
	s_and_b64 s[4:5], vcc, s[4:5]
	s_cmp_lt_i32 s38, s76
	s_waitcnt vmcnt(13)
	v_cndmask_b32_e64 v68, 0, v68, s[4:5]
	s_cselect_b64 s[4:5], -1, 0
	s_and_b64 s[4:5], vcc, s[4:5]
	s_cmp_lt_i32 s39, s76
	s_waitcnt vmcnt(12)
	v_cndmask_b32_e64 v67, 0, v67, s[4:5]
	s_cselect_b64 s[4:5], -1, 0
	s_and_b64 s[4:5], vcc, s[4:5]
	s_cmp_lt_i32 s34, s76
	s_waitcnt vmcnt(11)
	v_cndmask_b32_e64 v66, 0, v66, s[4:5]
	s_cselect_b64 s[4:5], -1, 0
	s_and_b64 s[4:5], vcc, s[4:5]
	s_cmp_lt_i32 s35, s76
	s_waitcnt vmcnt(10)
	v_cndmask_b32_e64 v64, 0, v64, s[4:5]
	s_cselect_b64 s[4:5], -1, 0
	s_and_b64 s[4:5], vcc, s[4:5]
	s_cmp_lt_i32 s42, s76
	s_waitcnt vmcnt(9)
	v_cndmask_b32_e64 v63, 0, v63, s[4:5]
	s_cselect_b64 s[4:5], -1, 0
	s_and_b64 s[4:5], vcc, s[4:5]
	s_cmp_lt_i32 s43, s76
	s_waitcnt vmcnt(8)
	v_cndmask_b32_e64 v62, 0, v62, s[4:5]
	s_cselect_b64 s[4:5], -1, 0
	s_and_b64 s[4:5], vcc, s[4:5]
	s_cmp_lt_i32 s54, s76
	s_waitcnt vmcnt(7)
	v_cndmask_b32_e64 v65, 0, v65, s[4:5]
	s_cselect_b64 s[4:5], -1, 0
	s_and_b64 s[4:5], vcc, s[4:5]
	s_cmp_lt_i32 s55, s76
	s_waitcnt vmcnt(6)
	v_cndmask_b32_e64 v74, 0, v74, s[4:5]
	s_cselect_b64 s[4:5], -1, 0
	s_and_b64 s[4:5], vcc, s[4:5]
	s_cmp_lt_i32 s46, s76
	ds_write2_b32 v12, v21, v20 offset1:65
	ds_write2_b32 v12, v19, v18 offset0:130 offset1:195
	v_add_u32_e32 v18, 0x400, v12
	s_waitcnt vmcnt(5)
	v_cndmask_b32_e64 v73, 0, v73, s[4:5]
	s_cselect_b64 s[4:5], -1, 0
	ds_write2_b32 v18, v17, v16 offset0:4 offset1:69
	ds_write2_b32 v18, v15, v8 offset0:134 offset1:199
	v_add_u32_e32 v8, 0x800, v12
	s_and_b64 s[4:5], vcc, s[4:5]
	ds_write2_b32 v8, v29, v28 offset0:8 offset1:73
	ds_write2_b32 v8, v27, v26 offset0:138 offset1:203
	v_add_u32_e32 v8, 0xc00, v12
	s_cmp_lt_i32 s47, s76
	ds_write2_b32 v8, v25, v24 offset0:12 offset1:77
	ds_write2_b32 v8, v23, v22 offset0:142 offset1:207
	v_add_u32_e32 v8, 0x1000, v12
	s_waitcnt vmcnt(4)
	v_cndmask_b32_e64 v72, 0, v72, s[4:5]
	s_cselect_b64 s[4:5], -1, 0
	ds_write2_b32 v8, v37, v36 offset0:16 offset1:81
	ds_write2_b32 v8, v35, v34 offset0:146 offset1:211
	v_add_u32_e32 v8, 0x1400, v12
	s_and_b64 s[4:5], vcc, s[4:5]
	ds_write2_b32 v8, v33, v32 offset0:20 offset1:85
	ds_write2_b32 v8, v31, v30 offset0:150 offset1:215
	v_add_u32_e32 v8, 0x1800, v12
	s_cmp_lt_i32 s48, s76
	ds_write2_b32 v8, v45, v44 offset0:24 offset1:89
	ds_write2_b32 v8, v43, v42 offset0:154 offset1:219
	v_add_u32_e32 v8, 0x1c00, v12
	s_waitcnt vmcnt(3)
	v_cndmask_b32_e64 v71, 0, v71, s[4:5]
	s_cselect_b64 s[4:5], -1, 0
	ds_write2_b32 v8, v41, v40 offset0:28 offset1:93
	ds_write2_b32 v8, v39, v38 offset0:158 offset1:223
	v_add_u32_e32 v8, 0x2000, v12
	s_and_b64 s[4:5], vcc, s[4:5]
	ds_write2_b32 v8, v53, v52 offset0:32 offset1:97
	ds_write2_b32 v8, v51, v50 offset0:162 offset1:227
	v_add_u32_e32 v8, 0x2400, v12
	s_cmp_lt_i32 s49, s76
	ds_write2_b32 v8, v49, v48 offset0:36 offset1:101
	ds_write2_b32 v8, v47, v46 offset0:166 offset1:231
	v_add_u32_e32 v8, 0x2800, v12
	s_waitcnt vmcnt(2)
	v_cndmask_b32_e64 v77, 0, v77, s[4:5]
	s_cselect_b64 s[4:5], -1, 0
	ds_write2_b32 v8, v61, v60 offset0:40 offset1:105
	ds_write2_b32 v8, v59, v58 offset0:170 offset1:235
	v_add_u32_e32 v8, 0x2c00, v12
	s_and_b64 s[4:5], vcc, s[4:5]
	ds_write2_b32 v8, v57, v56 offset0:44 offset1:109
	ds_write2_b32 v8, v55, v54 offset0:174 offset1:239
	v_add_u32_e32 v8, 0x3000, v12
	s_cmp_lt_i32 s44, s76
	ds_write2_b32 v8, v70, v69 offset0:48 offset1:113
	ds_write2_b32 v8, v68, v67 offset0:178 offset1:243
	v_add_u32_e32 v8, 0x3400, v12
	s_waitcnt vmcnt(1)
	v_cndmask_b32_e64 v76, 0, v76, s[4:5]
	s_cselect_b64 s[4:5], -1, 0
	ds_write2_b32 v8, v66, v64 offset0:52 offset1:117
	ds_write2_b32 v8, v63, v62 offset0:182 offset1:247
	v_add_u32_e32 v8, 0x3800, v12
	s_and_b64 vcc, vcc, s[4:5]
	ds_write2_b32 v8, v65, v74 offset0:56 offset1:121
	ds_write2_b32 v8, v73, v72 offset0:186 offset1:251
	v_add_u32_e32 v8, 0x3c00, v12
	s_waitcnt vmcnt(0)
	v_cndmask_b32_e32 v75, 0, v75, vcc
	ds_write2_b32 v8, v71, v77 offset0:60 offset1:125
	ds_write2_b32 v8, v76, v75 offset0:190 offset1:255
	s_waitcnt lgkmcnt(0)
	ds_read2_b32 v[16:17], v14 offset1:65
	v_add_u32_e32 v24, s59, v13
	v_mul_lo_u32 v22, s57, v24
	s_ashr_i32 s59, s58, 31
	v_readlane_b32 s76, v254, 31
	s_waitcnt lgkmcnt(0)
; __device__ __forceinline__ unsigned cvt_pk_bf16(float lo, float hi) { unsigned r; asm volatile("v_cvt_pk_bf16_f32 %0, %1, %2" : "=v"(r) : "v"(lo), "v"(hi)); return r; }
; #define LAS __attribute__((address_space(3)))
; #define LDS_WAIT() asm volatile("s_waitcnt lgkmcnt(0)" ::: "memory")
; __device__ __forceinline__ void conv_store(const ConvItem& ci, LAS float* scr, int lane, const float (&v)[64]) {
;     const int c = lane & 7;
;     f32x4 s0 = {1.f, 1.f, 1.f, 1.f}, s1 = s0;
;     if (ci.ks) { const int kb = ci.k0 + 8 * c < ci.Ksrc - 8 ? ci.k0 + 8 * c : ci.Ksrc - 8; s0 = *(const f32x4*)(ci.ks + kb); s1 = *(const f32x4*)(ci.ks + kb + 4); }
; #pragma unroll
;     for (int i = 0; i < 64; ++i) scr[i * 65 + lane] = v[i];
;     LDS_WAIT(); asm volatile("" ::: "memory");
; #pragma unroll
;     for (int j = 0; j < 8; ++j) { const int n = (lane >> 3) + 8 * j; const LAS float* s = scr + (8 * c) * 65 + n;
;         v4u o; o.x = cvt_pk_bf16(s[0 * 65] * s0[0], s[1 * 65] * s0[1]); o.y = cvt_pk_bf16(s[2 * 65] * s0[2], s[3 * 65] * s0[3]); o.z = cvt_pk_bf16(s[4 * 65] * s1[0], s[5 * 65] * s1[1]); o.w = cvt_pk_bf16(s[6 * 65] * s1[2], s[7 * 65] * s1[3]);
;         *(v4u*)(ci.dst + (size_t)(ci.drow0 + n) * ci.ldd + ci.k0 + 8 * c) = o; }
;     LDS_WAIT(); asm volatile("" ::: "memory");
	v_mul_f32_e32 v8, v4, v16
	v_mul_f32_e32 v15, v5, v17
	v_cvt_pk_bf16_f32 v16, v8, v15
	ds_read2_b32 v[18:19], v14 offset0:130 offset1:195
	s_add_i32 s3, s3, s33
	s_add_i32 s66, s66, s67
	s_add_i32 s68, s68, s69
	s_add_i32 s70, s70, s71
	s_waitcnt lgkmcnt(0)
	v_mul_f32_e32 v15, v7, v19
	v_mul_f32_e32 v8, v6, v18
	v_cvt_pk_bf16_f32 v17, v8, v15
	v_add_u32_e32 v15, 0x400, v14
	ds_read2_b32 v[18:19], v15 offset0:4 offset1:69
	s_add_i32 s72, s72, s73
	s_add_i32 s74, s74, s75
	v_readlane_b32 s78, v254, 33
	v_readlane_b32 s79, v254, 34
	s_waitcnt lgkmcnt(0)
	v_mul_f32_e32 v8, v0, v18
	v_mul_f32_e32 v18, v1, v19
	v_cvt_pk_bf16_f32 v18, v8, v18
	ds_read2_b32 v[20:21], v15 offset0:134 offset1:199
	v_readlane_b32 s80, v255, 21
	v_readlane_b32 s77, v254, 32
	s_movk_i32 s78, 0x1580
	v_readlane_b32 s82, v255, 23
	s_waitcnt lgkmcnt(0)
	v_mul_f32_e32 v8, v2, v20
	v_mul_f32_e32 v19, v3, v21
	v_cvt_pk_bf16_f32 v19, v8, v19
	v_ashrrev_i32_e32 v8, 31, v24
	v_mul_lo_u32 v8, s56, v8
	v_mad_u64_u32 v[20:21], s[4:5], s56, v24, 0
	v_add3_u32 v21, v21, v8, v22
	ds_read2_b32 v[22:23], v14 offset0:8 offset1:73
	v_lshl_add_u64 v[20:21], v[20:21], 1, s[60:61]
	s_lshl_b64 s[4:5], s[58:59], 1
	v_lshl_add_u64 v[20:21], v[20:21], 0, s[4:5]
	v_lshlrev_b32_e32 v8, 1, v10
	v_lshl_add_u64 v[20:21], v[20:21], 0, v[8:9]
	global_store_dwordx4 v[20:21], v[16:19], off
	s_cmpk_lt_i32 s3, 25216
	v_readlane_b32 s83, v255, 24
	s_waitcnt lgkmcnt(0)
	v_mul_f32_e32 v16, v4, v22
	v_mul_f32_e32 v17, v5, v23
	v_cvt_pk_bf16_f32 v16, v16, v17
	ds_read2_b32 v[18:19], v14 offset0:138 offset1:203
	s_mov_b32 s79, 0x3f22f983
	s_mov_b32 s85, 0xbfc90fda
	s_brev_b32 s86, 1
	s_movk_i32 s87, 0x1f8
	s_waitcnt lgkmcnt(0)
	v_mul_f32_e32 v17, v6, v18
	v_mul_f32_e32 v18, v7, v19
	v_cvt_pk_bf16_f32 v17, v17, v18
	ds_read2_b32 v[18:19], v15 offset0:12 offset1:77
	s_mov_b64 s[88:89], 0x80
	s_mov_b64 s[92:93], 0x4000
	s_mov_b64 s[94:95], 0x4800
	v_readlane_b32 s81, v255, 22
	s_waitcnt lgkmcnt(0)
	v_mul_f32_e32 v18, v0, v18
	v_mul_f32_e32 v19, v1, v19
	v_cvt_pk_bf16_f32 v18, v18, v19
	ds_read2_b32 v[20:21], v15 offset0:142 offset1:207
	s_waitcnt lgkmcnt(0)
	v_mul_f32_e32 v19, v2, v20
	v_mul_f32_e32 v20, v3, v21
	v_cvt_pk_bf16_f32 v19, v19, v20
	v_add_u32_e32 v20, 8, v24
	v_ashrrev_i32_e32 v21, 31, v20
	v_mul_lo_u32 v22, s56, v21
	v_mul_lo_u32 v23, s57, v20
	v_mad_u64_u32 v[20:21], s[6:7], s56, v20, 0
	v_add3_u32 v21, v21, v22, v23
	ds_read2_b32 v[22:23], v14 offset0:16 offset1:81
	v_lshl_add_u64 v[20:21], v[20:21], 1, s[60:61]
	v_lshl_add_u64 v[20:21], v[20:21], 0, s[4:5]
	v_lshl_add_u64 v[20:21], v[20:21], 0, v[8:9]
	global_store_dwordx4 v[20:21], v[16:19], off
	s_waitcnt lgkmcnt(0)
	s_nop 0
	v_mul_f32_e32 v16, v4, v22
	v_mul_f32_e32 v17, v5, v23
	v_cvt_pk_bf16_f32 v16, v16, v17
	ds_read2_b32 v[18:19], v14 offset0:146 offset1:211
	s_waitcnt lgkmcnt(0)
	v_mul_f32_e32 v17, v6, v18
	v_mul_f32_e32 v18, v7, v19
	v_cvt_pk_bf16_f32 v17, v17, v18
	ds_read2_b32 v[18:19], v15 offset0:20 offset1:85
	s_waitcnt lgkmcnt(0)
	v_mul_f32_e32 v18, v0, v18
	v_mul_f32_e32 v19, v1, v19
	v_cvt_pk_bf16_f32 v18, v18, v19
	ds_read2_b32 v[20:21], v15 offset0:150 offset1:215
	s_waitcnt lgkmcnt(0)
	v_mul_f32_e32 v19, v2, v20
	v_mul_f32_e32 v20, v3, v21
	v_cvt_pk_bf16_f32 v19, v19, v20
	v_add_u32_e32 v20, 16, v24
	v_ashrrev_i32_e32 v21, 31, v20
	v_mul_lo_u32 v22, s56, v21
	v_mul_lo_u32 v23, s57, v20
	v_mad_u64_u32 v[20:21], s[6:7], s56, v20, 0
	v_add3_u32 v21, v21, v22, v23
	ds_read2_b32 v[22:23], v14 offset0:24 offset1:89
	v_lshl_add_u64 v[20:21], v[20:21], 1, s[60:61]
	v_lshl_add_u64 v[20:21], v[20:21], 0, s[4:5]
	v_lshl_add_u64 v[20:21], v[20:21], 0, v[8:9]
	global_store_dwordx4 v[20:21], v[16:19], off
	s_waitcnt lgkmcnt(0)
	s_nop 0
	v_mul_f32_e32 v16, v4, v22
	v_mul_f32_e32 v17, v5, v23
	v_cvt_pk_bf16_f32 v16, v16, v17
	ds_read2_b32 v[18:19], v14 offset0:154 offset1:219
	s_waitcnt lgkmcnt(0)
	v_mul_f32_e32 v17, v6, v18
	v_mul_f32_e32 v18, v7, v19
	v_cvt_pk_bf16_f32 v17, v17, v18
	ds_read2_b32 v[18:19], v15 offset0:28 offset1:93
	s_waitcnt lgkmcnt(0)
	v_mul_f32_e32 v18, v0, v18
	v_mul_f32_e32 v19, v1, v19
	v_cvt_pk_bf16_f32 v18, v18, v19
	ds_read2_b32 v[20:21], v15 offset0:158 offset1:223
	s_waitcnt lgkmcnt(0)
; __device__ __forceinline__ unsigned cvt_pk_bf16(float lo, float hi) { unsigned r; asm volatile("v_cvt_pk_bf16_f32 %0, %1, %2" : "=v"(r) : "v"(lo), "v"(hi)); return r; }
; #define LAS __attribute__((address_space(3)))
; #define LDS_WAIT() asm volatile("s_waitcnt lgkmcnt(0)" ::: "memory")
; __device__ __forceinline__ void conv_store(const ConvItem& ci, LAS float* scr, int lane, const float (&v)[64]) {
;     ...
;     for (int j = 0; j < 8; ++j) { const int n = (lane >> 3) + 8 * j; const LAS float* s = scr + (8 * c) * 65 + n;
;         v4u o; o.x = cvt_pk_bf16(s[0 * 65] * s0[0], s[1 * 65] * s0[1]); o.y = cvt_pk_bf16(s[2 * 65] * s0[2], s[3 * 65] * s0[3]); o.z = cvt_pk_bf16(s[4 * 65] * s1[0], s[5 * 65] * s1[1]); o.w = cvt_pk_bf16(s[6 * 65] * s1[2], s[7 * 65] * s1[3]);
;         *(v4u*)(ci.dst + (size_t)(ci.drow0 + n) * ci.ldd + ci.k0 + 8 * c) = o; }
;     LDS_WAIT(); asm volatile("" ::: "memory");
	v_mul_f32_e32 v19, v2, v20
	v_mul_f32_e32 v20, v3, v21
	v_cvt_pk_bf16_f32 v19, v19, v20
	v_add_u32_e32 v20, 24, v24
	v_ashrrev_i32_e32 v21, 31, v20
	v_mul_lo_u32 v22, s56, v21
	v_mul_lo_u32 v23, s57, v20
	v_mad_u64_u32 v[20:21], s[6:7], s56, v20, 0
	v_add3_u32 v21, v21, v22, v23
	ds_read2_b32 v[22:23], v14 offset0:32 offset1:97
	v_lshl_add_u64 v[20:21], v[20:21], 1, s[60:61]
	v_lshl_add_u64 v[20:21], v[20:21], 0, s[4:5]
	v_lshl_add_u64 v[20:21], v[20:21], 0, v[8:9]
	global_store_dwordx4 v[20:21], v[16:19], off
	s_waitcnt lgkmcnt(0)
	s_nop 0
	v_mul_f32_e32 v16, v4, v22
	v_mul_f32_e32 v17, v5, v23
	v_cvt_pk_bf16_f32 v16, v16, v17
	ds_read2_b32 v[18:19], v14 offset0:162 offset1:227
	s_waitcnt lgkmcnt(0)
	v_mul_f32_e32 v17, v6, v18
	v_mul_f32_e32 v18, v7, v19
	v_cvt_pk_bf16_f32 v17, v17, v18
	ds_read2_b32 v[18:19], v15 offset0:36 offset1:101
	s_waitcnt lgkmcnt(0)
	v_mul_f32_e32 v18, v0, v18
	v_mul_f32_e32 v19, v1, v19
	v_cvt_pk_bf16_f32 v18, v18, v19
	ds_read2_b32 v[20:21], v15 offset0:166 offset1:231
	s_waitcnt lgkmcnt(0)
	v_mul_f32_e32 v19, v2, v20
	v_mul_f32_e32 v20, v3, v21
	v_cvt_pk_bf16_f32 v19, v19, v20
	v_add_u32_e32 v20, 32, v24
	v_ashrrev_i32_e32 v21, 31, v20
	v_mul_lo_u32 v22, s56, v21
	v_mul_lo_u32 v23, s57, v20
	v_mad_u64_u32 v[20:21], s[6:7], s56, v20, 0
	v_add3_u32 v21, v21, v22, v23
	ds_read2_b32 v[22:23], v14 offset0:40 offset1:105
	v_lshl_add_u64 v[20:21], v[20:21], 1, s[60:61]
	v_lshl_add_u64 v[20:21], v[20:21], 0, s[4:5]
	v_lshl_add_u64 v[20:21], v[20:21], 0, v[8:9]
	global_store_dwordx4 v[20:21], v[16:19], off
	s_waitcnt lgkmcnt(0)
	s_nop 0
	v_mul_f32_e32 v16, v4, v22
	v_mul_f32_e32 v17, v5, v23
	v_cvt_pk_bf16_f32 v16, v16, v17
	ds_read2_b32 v[18:19], v14 offset0:170 offset1:235
	s_waitcnt lgkmcnt(0)
	v_mul_f32_e32 v17, v6, v18
	v_mul_f32_e32 v18, v7, v19
	v_cvt_pk_bf16_f32 v17, v17, v18
	ds_read2_b32 v[18:19], v15 offset0:44 offset1:109
	s_waitcnt lgkmcnt(0)
	v_mul_f32_e32 v18, v0, v18
	v_mul_f32_e32 v19, v1, v19
	v_cvt_pk_bf16_f32 v18, v18, v19
	ds_read2_b32 v[20:21], v15 offset0:174 offset1:239
	s_waitcnt lgkmcnt(0)
	v_mul_f32_e32 v19, v2, v20
	v_mul_f32_e32 v20, v3, v21
	v_cvt_pk_bf16_f32 v19, v19, v20
	v_add_u32_e32 v20, 40, v24
	v_ashrrev_i32_e32 v21, 31, v20
	v_mul_lo_u32 v22, s56, v21
	v_mul_lo_u32 v23, s57, v20
	v_mad_u64_u32 v[20:21], s[6:7], s56, v20, 0
	v_add3_u32 v21, v21, v22, v23
	ds_read2_b32 v[22:23], v14 offset0:48 offset1:113
	v_lshl_add_u64 v[20:21], v[20:21], 1, s[60:61]
	v_lshl_add_u64 v[20:21], v[20:21], 0, s[4:5]
	v_lshl_add_u64 v[20:21], v[20:21], 0, v[8:9]
	global_store_dwordx4 v[20:21], v[16:19], off
	s_waitcnt lgkmcnt(0)
	s_nop 0
	v_mul_f32_e32 v16, v4, v22
	v_mul_f32_e32 v17, v5, v23
	v_cvt_pk_bf16_f32 v16, v16, v17
	ds_read2_b32 v[18:19], v14 offset0:178 offset1:243
	s_waitcnt lgkmcnt(0)
	v_mul_f32_e32 v17, v6, v18
	v_mul_f32_e32 v18, v7, v19
	v_cvt_pk_bf16_f32 v17, v17, v18
	ds_read2_b32 v[18:19], v15 offset0:52 offset1:117
	s_waitcnt lgkmcnt(0)
	v_mul_f32_e32 v18, v0, v18
	v_mul_f32_e32 v19, v1, v19
	v_cvt_pk_bf16_f32 v18, v18, v19
	ds_read2_b32 v[20:21], v15 offset0:182 offset1:247
	s_waitcnt lgkmcnt(0)
	v_mul_f32_e32 v19, v2, v20
	v_mul_f32_e32 v20, v3, v21
	v_cvt_pk_bf16_f32 v19, v19, v20
	v_add_u32_e32 v20, 48, v24
	v_ashrrev_i32_e32 v21, 31, v20
	v_mul_lo_u32 v22, s56, v21
	v_mul_lo_u32 v23, s57, v20
	v_mad_u64_u32 v[20:21], s[6:7], s56, v20, 0
	v_add3_u32 v21, v21, v22, v23
	ds_read2_b32 v[22:23], v14 offset0:56 offset1:121
	v_lshl_add_u64 v[20:21], v[20:21], 1, s[60:61]
	v_lshl_add_u64 v[20:21], v[20:21], 0, s[4:5]
	v_lshl_add_u64 v[20:21], v[20:21], 0, v[8:9]
	global_store_dwordx4 v[20:21], v[16:19], off
	s_waitcnt lgkmcnt(0)
	v_mul_f32_e32 v4, v4, v22
	v_mul_f32_e32 v5, v5, v23
	v_cvt_pk_bf16_f32 v4, v4, v5
	ds_read2_b32 v[16:17], v14 offset0:186 offset1:251
	s_waitcnt lgkmcnt(0)
	v_mul_f32_e32 v5, v6, v16
	v_mul_f32_e32 v6, v7, v17
	v_cvt_pk_bf16_f32 v5, v5, v6
	ds_read2_b32 v[6:7], v15 offset0:60 offset1:125
	s_waitcnt lgkmcnt(0)
	v_mul_f32_e32 v0, v0, v6
	v_mul_f32_e32 v1, v1, v7
	v_cvt_pk_bf16_f32 v6, v0, v1
	ds_read2_b32 v[0:1], v15 offset0:190 offset1:255
	s_waitcnt lgkmcnt(0)
	v_mul_f32_e32 v0, v2, v0
	v_mul_f32_e32 v1, v3, v1
	v_cvt_pk_bf16_f32 v7, v0, v1
	v_add_u32_e32 v0, 56, v24
	v_ashrrev_i32_e32 v1, 31, v0
	v_mul_lo_u32 v2, s56, v1
	v_mul_lo_u32 v3, s57, v0
	v_mad_u64_u32 v[0:1], s[6:7], s56, v0, 0
	v_add3_u32 v1, v1, v2, v3
	v_lshl_add_u64 v[0:1], v[0:1], 1, s[60:61]
	v_lshl_add_u64 v[0:1], v[0:1], 0, s[4:5]
	v_lshl_add_u64 v[0:1], v[0:1], 0, v[8:9]
	global_store_dwordx4 v[0:1], v[4:7], off
	s_waitcnt lgkmcnt(0)
	s_cbranch_scc0 .Lcvp31_ret
